# final combine: norm gains hoisted out of the row loop (no store-ack waits per row); cmp_finalize 4-row register-blocked fast path
# speedup vs baseline: 1.0179x; 1.0121x over previous
; #define LAS __attribute__((address_space(3)))
; __device__ __forceinline__ float gelu1(float x) { f32x2 r = gelu_pk((f32x2){x, 0.f}); return r.x; }
; #define FIN(i) kin(i)
; __device__ __forceinline__ void cmp_finalize_phase(Frame& F) {
;     const float* LOHI = (const float*)(F.ws + SC_LOHI); const float* cb = (const float*)(F.ws + SM_CBIAS); bf16* KC = (bf16*)(F.ws + SC_KC);
;     LAS float* hl = (LAS float*)(F.lds) + F.wave * 128;
;     const int gw = F.vcu * NWAVES + F.wave, NGW = F.G * NWAVES;
;     for (int r = gw; r < 2 * 8 * 1024; r += NGW) {
;         const int which = r >> 13, i = r & 1023; bf16* dst = KC + (size_t)r * HD; unsigned char* dst8 = (unsigned char*)KC + (size_t)r * HD;
;         if (i == 1023) { if (which) { dst[F.lane] = 0; dst[F.lane + 64] = 0; } else { dst8[F.lane] = 0; dst8[F.lane + 64] = 0; } continue; }
;         const float* w2 = FIN(which ? I_CVW2 : I_CKW2);
;         const float* lo = LOHI + (size_t)r * 256; const float* hi = lo + 256 + 128;
; #pragma unroll
;         for (int h = 0; h < 2; ++h) { const int n = F.lane + 64 * h; hl[n] = gelu1(lo[n] + hi[n] + cb[which * 128 + n]); }
.LBB0_1406:
	s_cmp_lt_i32 s92, 11
	s_cselect_b64 s[4:5], -1, 0
	s_and_b64 s[2:3], s[4:5], s[2:3]
	s_andn2_b64 vcc, exec, s[2:3]
	s_cbranch_vccnz .LBB0_1423
	s_lshl_b32 s2, s77, 3
	s_add_i32 s2, s2, s96
	s_cmpk_gt_i32 s2, 0x3fff
	s_cbranch_scc1 .LBB0_1423
	s_add_u32 s4, s28, 0x1440000
	s_addc_u32 s5, s29, 0
	s_add_u32 s18, s28, 0x37000000
	v_ashrrev_i32_e32 v33, 31, v32
	s_addc_u32 s19, s29, 0
	s_lshl_b32 s3, s96, 9
	s_waitcnt vmcnt(0)
	v_lshlrev_b64 v[0:1], 2, v[32:33]
	v_add_u32_e32 v4, 0x80, v32
	s_add_i32 s22, s3, 0
	v_lshl_add_u64 v[2:3], s[28:29], 0, v[0:1]
	s_mov_b64 s[6:7], 0x36000000
	v_ashrrev_i32_e32 v5, 31, v4
	s_lshl_b32 s23, s33, 3
	v_lshl_add_u32 v12, v32, 2, s22
	v_add_u32_e32 v13, 64, v32
	v_lshl_add_u64 v[2:3], v[2:3], 0, s[6:7]
	v_lshlrev_b64 v[4:5], 2, v[4:5]
	s_movk_i32 s24, 0x68
	v_mov_b32_e32 v14, 0xc0135761
	s_mov_b64 s[6:7], 0x1000
	s_movk_i32 s25, 0x7fff
	v_mov_b32_e32 v15, 0
	s_cmpk_lg_i32 s23, 0x800
	s_cbranch_scc1 .LBB0_1410
	s_mov_b32 s3, 0
	v_lshlrev_b32_e32 v64, 3, v32
	v_mov_b32_e32 v65, 0
	s_lshl_b32 s22, s96, 11
	v_lshl_add_u32 v234, v32, 3, s22
	v_mov_b32_e32 v235, s22
	s_mov_b64 s[6:7], 0x1000
.Lfin_pass:
	s_lshl_b32 s8, s3, 13
	s_add_i32 s8, s8, s2
	s_mul_i32 s9, s3, 0x18
	s_add_i32 s9, s9, 0xa8
	s_load_dwordx2 s[14:15], s[0:1], s9
	s_lshl_b32 s10, s3, 9
	s_mov_b32 s11, 0
	v_lshl_add_u64 v[66:67], s[4:5], 0, v[64:65]
	v_lshl_add_u64 v[66:67], v[66:67], 0, s[10:11]
	global_load_dwordx2 v[86:87], v[66:67], off
	s_lshl_b32 s10, s8, 10
	s_add_u32 s12, s28, 0x36000000
	s_addc_u32 s13, s29, 0
	s_add_u32 s12, s12, s10
	s_addc_u32 s13, s13, 0
	v_lshl_add_u64 v[68:69], s[12:13], 0, v[64:65]
	s_mov_b32 s10, 0x200000
	global_load_dwordx2 v[70:71], v[68:69], off
	global_load_dwordx2 v[72:73], v[68:69], off offset:1536
	v_lshl_add_u64 v[68:69], v[68:69], 0, s[10:11]
	global_load_dwordx2 v[74:75], v[68:69], off
	global_load_dwordx2 v[76:77], v[68:69], off offset:1536
	v_lshl_add_u64 v[68:69], v[68:69], 0, s[10:11]
	global_load_dwordx2 v[78:79], v[68:69], off
	global_load_dwordx2 v[80:81], v[68:69], off offset:1536
	v_lshl_add_u64 v[68:69], v[68:69], 0, s[10:11]
	global_load_dwordx2 v[82:83], v[68:69], off
	global_load_dwordx2 v[84:85], v[68:69], off offset:1536
	s_waitcnt lgkmcnt(0)
	v_lshl_add_u64 v[232:233], s[14:15], 0, v[64:65]
	global_load_dwordx2 v[104:105], v[232:233], off
	global_load_dwordx2 v[106:107], v[232:233], off offset:512
	global_load_dwordx2 v[108:109], v[232:233], off offset:1024
	global_load_dwordx2 v[110:111], v[232:233], off offset:1536
	global_load_dwordx2 v[112:113], v[232:233], off offset:2048
	global_load_dwordx2 v[114:115], v[232:233], off offset:2560
	global_load_dwordx2 v[116:117], v[232:233], off offset:3072
	global_load_dwordx2 v[118:119], v[232:233], off offset:3584
	v_lshl_add_u64 v[232:233], v[232:233], 0, s[6:7]
	global_load_dwordx2 v[120:121], v[232:233], off
	global_load_dwordx2 v[122:123], v[232:233], off offset:512
	global_load_dwordx2 v[124:125], v[232:233], off offset:1024
	global_load_dwordx2 v[126:127], v[232:233], off offset:1536
	global_load_dwordx2 v[128:129], v[232:233], off offset:2048
	global_load_dwordx2 v[130:131], v[232:233], off offset:2560
	global_load_dwordx2 v[132:133], v[232:233], off offset:3072
	global_load_dwordx2 v[134:135], v[232:233], off offset:3584
	v_lshl_add_u64 v[232:233], v[232:233], 0, s[6:7]
	global_load_dwordx2 v[136:137], v[232:233], off
	global_load_dwordx2 v[138:139], v[232:233], off offset:512
	global_load_dwordx2 v[140:141], v[232:233], off offset:1024
	global_load_dwordx2 v[142:143], v[232:233], off offset:1536
	global_load_dwordx2 v[144:145], v[232:233], off offset:2048
	global_load_dwordx2 v[146:147], v[232:233], off offset:2560
	global_load_dwordx2 v[148:149], v[232:233], off offset:3072
	global_load_dwordx2 v[150:151], v[232:233], off offset:3584
	v_lshl_add_u64 v[232:233], v[232:233], 0, s[6:7]
	global_load_dwordx2 v[152:153], v[232:233], off
	global_load_dwordx2 v[154:155], v[232:233], off offset:512
	global_load_dwordx2 v[156:157], v[232:233], off offset:1024
	global_load_dwordx2 v[158:159], v[232:233], off offset:1536
	global_load_dwordx2 v[160:161], v[232:233], off offset:2048
	global_load_dwordx2 v[162:163], v[232:233], off offset:2560
	global_load_dwordx2 v[164:165], v[232:233], off offset:3072
	global_load_dwordx2 v[166:167], v[232:233], off offset:3584
	v_lshl_add_u64 v[232:233], v[232:233], 0, s[6:7]
	s_waitcnt vmcnt(32)
; #define LDS_WAIT() asm volatile("s_waitcnt lgkmcnt(0)" ::: "memory")
; __device__ __forceinline__ f32x2 gelu_pk(f32x2 v) {
;     constexpr float C1 = -1.5957691216057308f * 1.4426950408889634f, C3 = C1 * 0.044715f;
;     const f32x2 z = v * ((v * v) * C3 + C1);
;     f32x2 e; e.x = __builtin_amdgcn_exp2f(z.x); e.y = __builtin_amdgcn_exp2f(z.y);
;     const f32x2 d = e + 1.0f;
;     f32x2 r; r.x = __builtin_amdgcn_rcpf(d.x); r.y = __builtin_amdgcn_rcpf(d.y);
;     return v * r;
; }
; __device__ __forceinline__ float gelu1(float x) { f32x2 r = gelu_pk((f32x2){x, 0.f}); return r.x; }
; __device__ __forceinline__ void cmp_finalize_phase(Frame& F) {
;     ...
;         for (int h = 0; h < 2; ++h) { const int n = F.lane + 64 * h; hl[n] = gelu1(lo[n] + hi[n] + cb[which * 128 + n]); }
;         LDS_WAIT(); asm volatile("" ::: "memory");
;         float a0 = 0.f, a1 = 0.f;
; #pragma unroll 8
;         for (int n = 0; n < 128; ++n) { const float h = hl[n]; a0 += h * w2[n * 128 + F.lane]; a1 += h * w2[n * 128 + 64 + F.lane]; }
	v_add_f32_e32 v88, v70, v72
	v_add_f32_e32 v89, v71, v73
	v_add_f32_e32 v90, v74, v76
	v_add_f32_e32 v91, v75, v77
	v_add_f32_e32 v92, v78, v80
	v_add_f32_e32 v93, v79, v81
	v_add_f32_e32 v94, v82, v84
	v_add_f32_e32 v95, v83, v85
	v_add_f32_e32 v88, v88, v86
	v_add_f32_e32 v89, v89, v87
	v_add_f32_e32 v90, v90, v86
	v_add_f32_e32 v91, v91, v87
	v_add_f32_e32 v92, v92, v86
	v_add_f32_e32 v93, v93, v87
	v_add_f32_e32 v94, v94, v86
	v_add_f32_e32 v95, v95, v87
	v_mul_f32_e32 v70, v88, v88
	v_mul_f32_e32 v71, v89, v89
	v_mul_f32_e32 v72, v90, v90
	v_mul_f32_e32 v73, v91, v91
	v_mul_f32_e32 v74, v92, v92
	v_mul_f32_e32 v75, v93, v93
	v_mul_f32_e32 v76, v94, v94
	v_mul_f32_e32 v77, v95, v95
	v_fmamk_f32 v70, v70, 0xbdd2d3e7, v14
	v_fmamk_f32 v71, v71, 0xbdd2d3e7, v14
	v_fmamk_f32 v72, v72, 0xbdd2d3e7, v14
	v_fmamk_f32 v73, v73, 0xbdd2d3e7, v14
	v_fmamk_f32 v74, v74, 0xbdd2d3e7, v14
	v_fmamk_f32 v75, v75, 0xbdd2d3e7, v14
	v_fmamk_f32 v76, v76, 0xbdd2d3e7, v14
	v_fmamk_f32 v77, v77, 0xbdd2d3e7, v14
	v_mul_f32_e32 v70, v88, v70
	v_mul_f32_e32 v71, v89, v71
	v_mul_f32_e32 v72, v90, v72
	v_mul_f32_e32 v73, v91, v73
	v_mul_f32_e32 v74, v92, v74
	v_mul_f32_e32 v75, v93, v75
	v_mul_f32_e32 v76, v94, v76
	v_mul_f32_e32 v77, v95, v77
	v_exp_f32_e32 v70, v70
	v_exp_f32_e32 v71, v71
	v_exp_f32_e32 v72, v72
	v_exp_f32_e32 v73, v73
	v_exp_f32_e32 v74, v74
	v_exp_f32_e32 v75, v75
	v_exp_f32_e32 v76, v76
	v_exp_f32_e32 v77, v77
	s_nop 0
	v_add_f32_e32 v70, 1.0, v70
	v_add_f32_e32 v71, 1.0, v71
	v_add_f32_e32 v72, 1.0, v72
	v_add_f32_e32 v73, 1.0, v73
	v_add_f32_e32 v74, 1.0, v74
	v_add_f32_e32 v75, 1.0, v75
	v_add_f32_e32 v76, 1.0, v76
	v_add_f32_e32 v77, 1.0, v77
	v_rcp_f32_e32 v70, v70
	v_rcp_f32_e32 v71, v71
	v_rcp_f32_e32 v72, v72
	v_rcp_f32_e32 v73, v73
	v_rcp_f32_e32 v74, v74
	v_rcp_f32_e32 v75, v75
	v_rcp_f32_e32 v76, v76
	v_rcp_f32_e32 v77, v77
	s_nop 0
	v_mul_f32_e32 v88, v88, v70
	v_mul_f32_e32 v89, v89, v71
	v_mul_f32_e32 v90, v90, v72
	v_mul_f32_e32 v91, v91, v73
	v_mul_f32_e32 v92, v92, v74
	v_mul_f32_e32 v93, v93, v75
	v_mul_f32_e32 v94, v94, v76
	v_mul_f32_e32 v95, v95, v77
	ds_write_b64 v234, v[88:89]
	ds_write_b64 v234, v[90:91] offset:512
	ds_write_b64 v234, v[92:93] offset:1024
	ds_write_b64 v234, v[94:95] offset:1536
	v_mov_b32_e32 v96, 0
	v_mov_b32_e32 v97, 0
	v_mov_b32_e32 v98, 0
	v_mov_b32_e32 v99, 0
	v_mov_b32_e32 v100, 0
	v_mov_b32_e32 v101, 0
	v_mov_b32_e32 v102, 0
	v_mov_b32_e32 v103, 0
	s_waitcnt lgkmcnt(0)
	ds_read_b128 v[168:171], v235 offset:0
	ds_read_b128 v[172:175], v235 offset:16
	ds_read_b128 v[176:179], v235 offset:32
	ds_read_b128 v[180:183], v235 offset:48
	ds_read_b128 v[184:187], v235 offset:512
	ds_read_b128 v[188:191], v235 offset:528
	ds_read_b128 v[192:195], v235 offset:544
	ds_read_b128 v[196:199], v235 offset:560
	ds_read_b128 v[200:203], v235 offset:1024
	ds_read_b128 v[204:207], v235 offset:1040
	ds_read_b128 v[208:211], v235 offset:1056
	ds_read_b128 v[212:215], v235 offset:1072
	ds_read_b128 v[216:219], v235 offset:1536
	ds_read_b128 v[220:223], v235 offset:1552
	ds_read_b128 v[224:227], v235 offset:1568
	ds_read_b128 v[228:231], v235 offset:1584
	s_waitcnt vmcnt(16)
	s_waitcnt lgkmcnt(0)
	v_pk_fma_f32 v[96:97], v[168:169], v[104:105], v[96:97] op_sel_hi:[0,1,1]
	v_pk_fma_f32 v[98:99], v[184:185], v[104:105], v[98:99] op_sel_hi:[0,1,1]
	v_pk_fma_f32 v[100:101], v[200:201], v[104:105], v[100:101] op_sel_hi:[0,1,1]
	v_pk_fma_f32 v[102:103], v[216:217], v[104:105], v[102:103] op_sel_hi:[0,1,1]
	v_pk_fma_f32 v[96:97], v[168:169], v[106:107], v[96:97] op_sel:[1,0,0]
	v_pk_fma_f32 v[98:99], v[184:185], v[106:107], v[98:99] op_sel:[1,0,0]
	v_pk_fma_f32 v[100:101], v[200:201], v[106:107], v[100:101] op_sel:[1,0,0]
	v_pk_fma_f32 v[102:103], v[216:217], v[106:107], v[102:103] op_sel:[1,0,0]
	v_pk_fma_f32 v[96:97], v[170:171], v[108:109], v[96:97] op_sel_hi:[0,1,1]
	v_pk_fma_f32 v[98:99], v[186:187], v[108:109], v[98:99] op_sel_hi:[0,1,1]
	v_pk_fma_f32 v[100:101], v[202:203], v[108:109], v[100:101] op_sel_hi:[0,1,1]
	v_pk_fma_f32 v[102:103], v[218:219], v[108:109], v[102:103] op_sel_hi:[0,1,1]
	v_pk_fma_f32 v[96:97], v[170:171], v[110:111], v[96:97] op_sel:[1,0,0]
	v_pk_fma_f32 v[98:99], v[186:187], v[110:111], v[98:99] op_sel:[1,0,0]
	v_pk_fma_f32 v[100:101], v[202:203], v[110:111], v[100:101] op_sel:[1,0,0]
	v_pk_fma_f32 v[102:103], v[218:219], v[110:111], v[102:103] op_sel:[1,0,0]
	v_pk_fma_f32 v[96:97], v[172:173], v[112:113], v[96:97] op_sel_hi:[0,1,1]
	v_pk_fma_f32 v[98:99], v[188:189], v[112:113], v[98:99] op_sel_hi:[0,1,1]
	v_pk_fma_f32 v[100:101], v[204:205], v[112:113], v[100:101] op_sel_hi:[0,1,1]
	v_pk_fma_f32 v[102:103], v[220:221], v[112:113], v[102:103] op_sel_hi:[0,1,1]
	v_pk_fma_f32 v[96:97], v[172:173], v[114:115], v[96:97] op_sel:[1,0,0]
	v_pk_fma_f32 v[98:99], v[188:189], v[114:115], v[98:99] op_sel:[1,0,0]
	v_pk_fma_f32 v[100:101], v[204:205], v[114:115], v[100:101] op_sel:[1,0,0]
	v_pk_fma_f32 v[102:103], v[220:221], v[114:115], v[102:103] op_sel:[1,0,0]
	v_pk_fma_f32 v[96:97], v[174:175], v[116:117], v[96:97] op_sel_hi:[0,1,1]
	v_pk_fma_f32 v[98:99], v[190:191], v[116:117], v[98:99] op_sel_hi:[0,1,1]
	v_pk_fma_f32 v[100:101], v[206:207], v[116:117], v[100:101] op_sel_hi:[0,1,1]
	v_pk_fma_f32 v[102:103], v[222:223], v[116:117], v[102:103] op_sel_hi:[0,1,1]
	v_pk_fma_f32 v[96:97], v[174:175], v[118:119], v[96:97] op_sel:[1,0,0]
	v_pk_fma_f32 v[98:99], v[190:191], v[118:119], v[98:99] op_sel:[1,0,0]
	v_pk_fma_f32 v[100:101], v[206:207], v[118:119], v[100:101] op_sel:[1,0,0]
	v_pk_fma_f32 v[102:103], v[222:223], v[118:119], v[102:103] op_sel:[1,0,0]
	v_pk_fma_f32 v[96:97], v[176:177], v[120:121], v[96:97] op_sel_hi:[0,1,1]
; __device__ __forceinline__ void cmp_finalize_phase(Frame& F) {
;     ...
;         float a0 = 0.f, a1 = 0.f;
; #pragma unroll 8
;         for (int n = 0; n < 128; ++n) { const float h = hl[n]; a0 += h * w2[n * 128 + F.lane]; a1 += h * w2[n * 128 + 64 + F.lane]; }
	v_pk_fma_f32 v[98:99], v[192:193], v[120:121], v[98:99] op_sel_hi:[0,1,1]
	v_pk_fma_f32 v[100:101], v[208:209], v[120:121], v[100:101] op_sel_hi:[0,1,1]
	v_pk_fma_f32 v[102:103], v[224:225], v[120:121], v[102:103] op_sel_hi:[0,1,1]
	v_pk_fma_f32 v[96:97], v[176:177], v[122:123], v[96:97] op_sel:[1,0,0]
	v_pk_fma_f32 v[98:99], v[192:193], v[122:123], v[98:99] op_sel:[1,0,0]
	v_pk_fma_f32 v[100:101], v[208:209], v[122:123], v[100:101] op_sel:[1,0,0]
	v_pk_fma_f32 v[102:103], v[224:225], v[122:123], v[102:103] op_sel:[1,0,0]
	v_pk_fma_f32 v[96:97], v[178:179], v[124:125], v[96:97] op_sel_hi:[0,1,1]
	v_pk_fma_f32 v[98:99], v[194:195], v[124:125], v[98:99] op_sel_hi:[0,1,1]
	v_pk_fma_f32 v[100:101], v[210:211], v[124:125], v[100:101] op_sel_hi:[0,1,1]
	v_pk_fma_f32 v[102:103], v[226:227], v[124:125], v[102:103] op_sel_hi:[0,1,1]
	v_pk_fma_f32 v[96:97], v[178:179], v[126:127], v[96:97] op_sel:[1,0,0]
	v_pk_fma_f32 v[98:99], v[194:195], v[126:127], v[98:99] op_sel:[1,0,0]
	v_pk_fma_f32 v[100:101], v[210:211], v[126:127], v[100:101] op_sel:[1,0,0]
	v_pk_fma_f32 v[102:103], v[226:227], v[126:127], v[102:103] op_sel:[1,0,0]
	v_pk_fma_f32 v[96:97], v[180:181], v[128:129], v[96:97] op_sel_hi:[0,1,1]
	v_pk_fma_f32 v[98:99], v[196:197], v[128:129], v[98:99] op_sel_hi:[0,1,1]
	v_pk_fma_f32 v[100:101], v[212:213], v[128:129], v[100:101] op_sel_hi:[0,1,1]
	v_pk_fma_f32 v[102:103], v[228:229], v[128:129], v[102:103] op_sel_hi:[0,1,1]
	v_pk_fma_f32 v[96:97], v[180:181], v[130:131], v[96:97] op_sel:[1,0,0]
	v_pk_fma_f32 v[98:99], v[196:197], v[130:131], v[98:99] op_sel:[1,0,0]
	v_pk_fma_f32 v[100:101], v[212:213], v[130:131], v[100:101] op_sel:[1,0,0]
	v_pk_fma_f32 v[102:103], v[228:229], v[130:131], v[102:103] op_sel:[1,0,0]
	v_pk_fma_f32 v[96:97], v[182:183], v[132:133], v[96:97] op_sel_hi:[0,1,1]
	v_pk_fma_f32 v[98:99], v[198:199], v[132:133], v[98:99] op_sel_hi:[0,1,1]
	v_pk_fma_f32 v[100:101], v[214:215], v[132:133], v[100:101] op_sel_hi:[0,1,1]
	v_pk_fma_f32 v[102:103], v[230:231], v[132:133], v[102:103] op_sel_hi:[0,1,1]
	v_pk_fma_f32 v[96:97], v[182:183], v[134:135], v[96:97] op_sel:[1,0,0]
	v_pk_fma_f32 v[98:99], v[198:199], v[134:135], v[98:99] op_sel:[1,0,0]
	v_pk_fma_f32 v[100:101], v[214:215], v[134:135], v[100:101] op_sel:[1,0,0]
	v_pk_fma_f32 v[102:103], v[230:231], v[134:135], v[102:103] op_sel:[1,0,0]
	global_load_dwordx2 v[104:105], v[232:233], off
	global_load_dwordx2 v[106:107], v[232:233], off offset:512
	global_load_dwordx2 v[108:109], v[232:233], off offset:1024
	global_load_dwordx2 v[110:111], v[232:233], off offset:1536
	global_load_dwordx2 v[112:113], v[232:233], off offset:2048
	global_load_dwordx2 v[114:115], v[232:233], off offset:2560
	global_load_dwordx2 v[116:117], v[232:233], off offset:3072
	global_load_dwordx2 v[118:119], v[232:233], off offset:3584
	v_lshl_add_u64 v[232:233], v[232:233], 0, s[6:7]
	global_load_dwordx2 v[120:121], v[232:233], off
	global_load_dwordx2 v[122:123], v[232:233], off offset:512
	global_load_dwordx2 v[124:125], v[232:233], off offset:1024
	global_load_dwordx2 v[126:127], v[232:233], off offset:1536
	global_load_dwordx2 v[128:129], v[232:233], off offset:2048
	global_load_dwordx2 v[130:131], v[232:233], off offset:2560
	global_load_dwordx2 v[132:133], v[232:233], off offset:3072
	global_load_dwordx2 v[134:135], v[232:233], off offset:3584
	v_lshl_add_u64 v[232:233], v[232:233], 0, s[6:7]
	ds_read_b128 v[168:171], v235 offset:64
	ds_read_b128 v[172:175], v235 offset:80
	ds_read_b128 v[176:179], v235 offset:96
	ds_read_b128 v[180:183], v235 offset:112
	ds_read_b128 v[184:187], v235 offset:576
	ds_read_b128 v[188:191], v235 offset:592
	ds_read_b128 v[192:195], v235 offset:608
	ds_read_b128 v[196:199], v235 offset:624
	ds_read_b128 v[200:203], v235 offset:1088
	ds_read_b128 v[204:207], v235 offset:1104
	ds_read_b128 v[208:211], v235 offset:1120
	ds_read_b128 v[212:215], v235 offset:1136
	ds_read_b128 v[216:219], v235 offset:1600
	ds_read_b128 v[220:223], v235 offset:1616
	ds_read_b128 v[224:227], v235 offset:1632
	ds_read_b128 v[228:231], v235 offset:1648
	s_waitcnt vmcnt(16)
	s_waitcnt lgkmcnt(0)
	v_pk_fma_f32 v[96:97], v[168:169], v[136:137], v[96:97] op_sel_hi:[0,1,1]
	v_pk_fma_f32 v[98:99], v[184:185], v[136:137], v[98:99] op_sel_hi:[0,1,1]
	v_pk_fma_f32 v[100:101], v[200:201], v[136:137], v[100:101] op_sel_hi:[0,1,1]
	v_pk_fma_f32 v[102:103], v[216:217], v[136:137], v[102:103] op_sel_hi:[0,1,1]
	v_pk_fma_f32 v[96:97], v[168:169], v[138:139], v[96:97] op_sel:[1,0,0]
	v_pk_fma_f32 v[98:99], v[184:185], v[138:139], v[98:99] op_sel:[1,0,0]
	v_pk_fma_f32 v[100:101], v[200:201], v[138:139], v[100:101] op_sel:[1,0,0]
	v_pk_fma_f32 v[102:103], v[216:217], v[138:139], v[102:103] op_sel:[1,0,0]
	v_pk_fma_f32 v[96:97], v[170:171], v[140:141], v[96:97] op_sel_hi:[0,1,1]
	v_pk_fma_f32 v[98:99], v[186:187], v[140:141], v[98:99] op_sel_hi:[0,1,1]
	v_pk_fma_f32 v[100:101], v[202:203], v[140:141], v[100:101] op_sel_hi:[0,1,1]
	v_pk_fma_f32 v[102:103], v[218:219], v[140:141], v[102:103] op_sel_hi:[0,1,1]
	v_pk_fma_f32 v[96:97], v[170:171], v[142:143], v[96:97] op_sel:[1,0,0]
	v_pk_fma_f32 v[98:99], v[186:187], v[142:143], v[98:99] op_sel:[1,0,0]
	v_pk_fma_f32 v[100:101], v[202:203], v[142:143], v[100:101] op_sel:[1,0,0]
	v_pk_fma_f32 v[102:103], v[218:219], v[142:143], v[102:103] op_sel:[1,0,0]
	v_pk_fma_f32 v[96:97], v[172:173], v[144:145], v[96:97] op_sel_hi:[0,1,1]
	v_pk_fma_f32 v[98:99], v[188:189], v[144:145], v[98:99] op_sel_hi:[0,1,1]
	v_pk_fma_f32 v[100:101], v[204:205], v[144:145], v[100:101] op_sel_hi:[0,1,1]
	v_pk_fma_f32 v[102:103], v[220:221], v[144:145], v[102:103] op_sel_hi:[0,1,1]
; __device__ __forceinline__ void cmp_finalize_phase(Frame& F) {
;     ...
;         float a0 = 0.f, a1 = 0.f;
; #pragma unroll 8
;         for (int n = 0; n < 128; ++n) { const float h = hl[n]; a0 += h * w2[n * 128 + F.lane]; a1 += h * w2[n * 128 + 64 + F.lane]; }
	v_pk_fma_f32 v[96:97], v[172:173], v[146:147], v[96:97] op_sel:[1,0,0]
	v_pk_fma_f32 v[98:99], v[188:189], v[146:147], v[98:99] op_sel:[1,0,0]
	v_pk_fma_f32 v[100:101], v[204:205], v[146:147], v[100:101] op_sel:[1,0,0]
	v_pk_fma_f32 v[102:103], v[220:221], v[146:147], v[102:103] op_sel:[1,0,0]
	v_pk_fma_f32 v[96:97], v[174:175], v[148:149], v[96:97] op_sel_hi:[0,1,1]
	v_pk_fma_f32 v[98:99], v[190:191], v[148:149], v[98:99] op_sel_hi:[0,1,1]
	v_pk_fma_f32 v[100:101], v[206:207], v[148:149], v[100:101] op_sel_hi:[0,1,1]
	v_pk_fma_f32 v[102:103], v[222:223], v[148:149], v[102:103] op_sel_hi:[0,1,1]
	v_pk_fma_f32 v[96:97], v[174:175], v[150:151], v[96:97] op_sel:[1,0,0]
	v_pk_fma_f32 v[98:99], v[190:191], v[150:151], v[98:99] op_sel:[1,0,0]
	v_pk_fma_f32 v[100:101], v[206:207], v[150:151], v[100:101] op_sel:[1,0,0]
	v_pk_fma_f32 v[102:103], v[222:223], v[150:151], v[102:103] op_sel:[1,0,0]
	v_pk_fma_f32 v[96:97], v[176:177], v[152:153], v[96:97] op_sel_hi:[0,1,1]
	v_pk_fma_f32 v[98:99], v[192:193], v[152:153], v[98:99] op_sel_hi:[0,1,1]
	v_pk_fma_f32 v[100:101], v[208:209], v[152:153], v[100:101] op_sel_hi:[0,1,1]
	v_pk_fma_f32 v[102:103], v[224:225], v[152:153], v[102:103] op_sel_hi:[0,1,1]
	v_pk_fma_f32 v[96:97], v[176:177], v[154:155], v[96:97] op_sel:[1,0,0]
	v_pk_fma_f32 v[98:99], v[192:193], v[154:155], v[98:99] op_sel:[1,0,0]
	v_pk_fma_f32 v[100:101], v[208:209], v[154:155], v[100:101] op_sel:[1,0,0]
	v_pk_fma_f32 v[102:103], v[224:225], v[154:155], v[102:103] op_sel:[1,0,0]
	v_pk_fma_f32 v[96:97], v[178:179], v[156:157], v[96:97] op_sel_hi:[0,1,1]
	v_pk_fma_f32 v[98:99], v[194:195], v[156:157], v[98:99] op_sel_hi:[0,1,1]
	v_pk_fma_f32 v[100:101], v[210:211], v[156:157], v[100:101] op_sel_hi:[0,1,1]
	v_pk_fma_f32 v[102:103], v[226:227], v[156:157], v[102:103] op_sel_hi:[0,1,1]
	v_pk_fma_f32 v[96:97], v[178:179], v[158:159], v[96:97] op_sel:[1,0,0]
	v_pk_fma_f32 v[98:99], v[194:195], v[158:159], v[98:99] op_sel:[1,0,0]
	v_pk_fma_f32 v[100:101], v[210:211], v[158:159], v[100:101] op_sel:[1,0,0]
	v_pk_fma_f32 v[102:103], v[226:227], v[158:159], v[102:103] op_sel:[1,0,0]
	v_pk_fma_f32 v[96:97], v[180:181], v[160:161], v[96:97] op_sel_hi:[0,1,1]
	v_pk_fma_f32 v[98:99], v[196:197], v[160:161], v[98:99] op_sel_hi:[0,1,1]
	v_pk_fma_f32 v[100:101], v[212:213], v[160:161], v[100:101] op_sel_hi:[0,1,1]
	v_pk_fma_f32 v[102:103], v[228:229], v[160:161], v[102:103] op_sel_hi:[0,1,1]
	v_pk_fma_f32 v[96:97], v[180:181], v[162:163], v[96:97] op_sel:[1,0,0]
	v_pk_fma_f32 v[98:99], v[196:197], v[162:163], v[98:99] op_sel:[1,0,0]
	v_pk_fma_f32 v[100:101], v[212:213], v[162:163], v[100:101] op_sel:[1,0,0]
	v_pk_fma_f32 v[102:103], v[228:229], v[162:163], v[102:103] op_sel:[1,0,0]
	v_pk_fma_f32 v[96:97], v[182:183], v[164:165], v[96:97] op_sel_hi:[0,1,1]
	v_pk_fma_f32 v[98:99], v[198:199], v[164:165], v[98:99] op_sel_hi:[0,1,1]
	v_pk_fma_f32 v[100:101], v[214:215], v[164:165], v[100:101] op_sel_hi:[0,1,1]
	v_pk_fma_f32 v[102:103], v[230:231], v[164:165], v[102:103] op_sel_hi:[0,1,1]
	v_pk_fma_f32 v[96:97], v[182:183], v[166:167], v[96:97] op_sel:[1,0,0]
	v_pk_fma_f32 v[98:99], v[198:199], v[166:167], v[98:99] op_sel:[1,0,0]
	v_pk_fma_f32 v[100:101], v[214:215], v[166:167], v[100:101] op_sel:[1,0,0]
	v_pk_fma_f32 v[102:103], v[230:231], v[166:167], v[102:103] op_sel:[1,0,0]
	global_load_dwordx2 v[136:137], v[232:233], off
	global_load_dwordx2 v[138:139], v[232:233], off offset:512
	global_load_dwordx2 v[140:141], v[232:233], off offset:1024
	global_load_dwordx2 v[142:143], v[232:233], off offset:1536
	global_load_dwordx2 v[144:145], v[232:233], off offset:2048
	global_load_dwordx2 v[146:147], v[232:233], off offset:2560
	global_load_dwordx2 v[148:149], v[232:233], off offset:3072
	global_load_dwordx2 v[150:151], v[232:233], off offset:3584
	v_lshl_add_u64 v[232:233], v[232:233], 0, s[6:7]
	global_load_dwordx2 v[152:153], v[232:233], off
	global_load_dwordx2 v[154:155], v[232:233], off offset:512
	global_load_dwordx2 v[156:157], v[232:233], off offset:1024
	global_load_dwordx2 v[158:159], v[232:233], off offset:1536
	global_load_dwordx2 v[160:161], v[232:233], off offset:2048
	global_load_dwordx2 v[162:163], v[232:233], off offset:2560
	global_load_dwordx2 v[164:165], v[232:233], off offset:3072
	global_load_dwordx2 v[166:167], v[232:233], off offset:3584
	v_lshl_add_u64 v[232:233], v[232:233], 0, s[6:7]
	ds_read_b128 v[168:171], v235 offset:128
	ds_read_b128 v[172:175], v235 offset:144
	ds_read_b128 v[176:179], v235 offset:160
	ds_read_b128 v[180:183], v235 offset:176
	ds_read_b128 v[184:187], v235 offset:640
	ds_read_b128 v[188:191], v235 offset:656
	ds_read_b128 v[192:195], v235 offset:672
	ds_read_b128 v[196:199], v235 offset:688
	ds_read_b128 v[200:203], v235 offset:1152
	ds_read_b128 v[204:207], v235 offset:1168
	ds_read_b128 v[208:211], v235 offset:1184
	ds_read_b128 v[212:215], v235 offset:1200
	ds_read_b128 v[216:219], v235 offset:1664
	ds_read_b128 v[220:223], v235 offset:1680
	ds_read_b128 v[224:227], v235 offset:1696
	ds_read_b128 v[228:231], v235 offset:1712
	s_waitcnt vmcnt(16)
	s_waitcnt lgkmcnt(0)
; __device__ __forceinline__ void cmp_finalize_phase(Frame& F) {
;     ...
;         float a0 = 0.f, a1 = 0.f;
; #pragma unroll 8
;         for (int n = 0; n < 128; ++n) { const float h = hl[n]; a0 += h * w2[n * 128 + F.lane]; a1 += h * w2[n * 128 + 64 + F.lane]; }
	v_pk_fma_f32 v[96:97], v[168:169], v[104:105], v[96:97] op_sel_hi:[0,1,1]
	v_pk_fma_f32 v[98:99], v[184:185], v[104:105], v[98:99] op_sel_hi:[0,1,1]
	v_pk_fma_f32 v[100:101], v[200:201], v[104:105], v[100:101] op_sel_hi:[0,1,1]
	v_pk_fma_f32 v[102:103], v[216:217], v[104:105], v[102:103] op_sel_hi:[0,1,1]
	v_pk_fma_f32 v[96:97], v[168:169], v[106:107], v[96:97] op_sel:[1,0,0]
	v_pk_fma_f32 v[98:99], v[184:185], v[106:107], v[98:99] op_sel:[1,0,0]
	v_pk_fma_f32 v[100:101], v[200:201], v[106:107], v[100:101] op_sel:[1,0,0]
	v_pk_fma_f32 v[102:103], v[216:217], v[106:107], v[102:103] op_sel:[1,0,0]
	v_pk_fma_f32 v[96:97], v[170:171], v[108:109], v[96:97] op_sel_hi:[0,1,1]
	v_pk_fma_f32 v[98:99], v[186:187], v[108:109], v[98:99] op_sel_hi:[0,1,1]
	v_pk_fma_f32 v[100:101], v[202:203], v[108:109], v[100:101] op_sel_hi:[0,1,1]
	v_pk_fma_f32 v[102:103], v[218:219], v[108:109], v[102:103] op_sel_hi:[0,1,1]
	v_pk_fma_f32 v[96:97], v[170:171], v[110:111], v[96:97] op_sel:[1,0,0]
	v_pk_fma_f32 v[98:99], v[186:187], v[110:111], v[98:99] op_sel:[1,0,0]
	v_pk_fma_f32 v[100:101], v[202:203], v[110:111], v[100:101] op_sel:[1,0,0]
	v_pk_fma_f32 v[102:103], v[218:219], v[110:111], v[102:103] op_sel:[1,0,0]
	v_pk_fma_f32 v[96:97], v[172:173], v[112:113], v[96:97] op_sel_hi:[0,1,1]
	v_pk_fma_f32 v[98:99], v[188:189], v[112:113], v[98:99] op_sel_hi:[0,1,1]
	v_pk_fma_f32 v[100:101], v[204:205], v[112:113], v[100:101] op_sel_hi:[0,1,1]
	v_pk_fma_f32 v[102:103], v[220:221], v[112:113], v[102:103] op_sel_hi:[0,1,1]
	v_pk_fma_f32 v[96:97], v[172:173], v[114:115], v[96:97] op_sel:[1,0,0]
	v_pk_fma_f32 v[98:99], v[188:189], v[114:115], v[98:99] op_sel:[1,0,0]
	v_pk_fma_f32 v[100:101], v[204:205], v[114:115], v[100:101] op_sel:[1,0,0]
	v_pk_fma_f32 v[102:103], v[220:221], v[114:115], v[102:103] op_sel:[1,0,0]
	v_pk_fma_f32 v[96:97], v[174:175], v[116:117], v[96:97] op_sel_hi:[0,1,1]
	v_pk_fma_f32 v[98:99], v[190:191], v[116:117], v[98:99] op_sel_hi:[0,1,1]
	v_pk_fma_f32 v[100:101], v[206:207], v[116:117], v[100:101] op_sel_hi:[0,1,1]
	v_pk_fma_f32 v[102:103], v[222:223], v[116:117], v[102:103] op_sel_hi:[0,1,1]
	v_pk_fma_f32 v[96:97], v[174:175], v[118:119], v[96:97] op_sel:[1,0,0]
	v_pk_fma_f32 v[98:99], v[190:191], v[118:119], v[98:99] op_sel:[1,0,0]
	v_pk_fma_f32 v[100:101], v[206:207], v[118:119], v[100:101] op_sel:[1,0,0]
	v_pk_fma_f32 v[102:103], v[222:223], v[118:119], v[102:103] op_sel:[1,0,0]
	v_pk_fma_f32 v[96:97], v[176:177], v[120:121], v[96:97] op_sel_hi:[0,1,1]
	v_pk_fma_f32 v[98:99], v[192:193], v[120:121], v[98:99] op_sel_hi:[0,1,1]
	v_pk_fma_f32 v[100:101], v[208:209], v[120:121], v[100:101] op_sel_hi:[0,1,1]
	v_pk_fma_f32 v[102:103], v[224:225], v[120:121], v[102:103] op_sel_hi:[0,1,1]
	v_pk_fma_f32 v[96:97], v[176:177], v[122:123], v[96:97] op_sel:[1,0,0]
	v_pk_fma_f32 v[98:99], v[192:193], v[122:123], v[98:99] op_sel:[1,0,0]
	v_pk_fma_f32 v[100:101], v[208:209], v[122:123], v[100:101] op_sel:[1,0,0]
	v_pk_fma_f32 v[102:103], v[224:225], v[122:123], v[102:103] op_sel:[1,0,0]
	v_pk_fma_f32 v[96:97], v[178:179], v[124:125], v[96:97] op_sel_hi:[0,1,1]
	v_pk_fma_f32 v[98:99], v[194:195], v[124:125], v[98:99] op_sel_hi:[0,1,1]
	v_pk_fma_f32 v[100:101], v[210:211], v[124:125], v[100:101] op_sel_hi:[0,1,1]
	v_pk_fma_f32 v[102:103], v[226:227], v[124:125], v[102:103] op_sel_hi:[0,1,1]
	v_pk_fma_f32 v[96:97], v[178:179], v[126:127], v[96:97] op_sel:[1,0,0]
	v_pk_fma_f32 v[98:99], v[194:195], v[126:127], v[98:99] op_sel:[1,0,0]
	v_pk_fma_f32 v[100:101], v[210:211], v[126:127], v[100:101] op_sel:[1,0,0]
	v_pk_fma_f32 v[102:103], v[226:227], v[126:127], v[102:103] op_sel:[1,0,0]
	v_pk_fma_f32 v[96:97], v[180:181], v[128:129], v[96:97] op_sel_hi:[0,1,1]
	v_pk_fma_f32 v[98:99], v[196:197], v[128:129], v[98:99] op_sel_hi:[0,1,1]
	v_pk_fma_f32 v[100:101], v[212:213], v[128:129], v[100:101] op_sel_hi:[0,1,1]
	v_pk_fma_f32 v[102:103], v[228:229], v[128:129], v[102:103] op_sel_hi:[0,1,1]
	v_pk_fma_f32 v[96:97], v[180:181], v[130:131], v[96:97] op_sel:[1,0,0]
	v_pk_fma_f32 v[98:99], v[196:197], v[130:131], v[98:99] op_sel:[1,0,0]
	v_pk_fma_f32 v[100:101], v[212:213], v[130:131], v[100:101] op_sel:[1,0,0]
	v_pk_fma_f32 v[102:103], v[228:229], v[130:131], v[102:103] op_sel:[1,0,0]
	v_pk_fma_f32 v[96:97], v[182:183], v[132:133], v[96:97] op_sel_hi:[0,1,1]
	v_pk_fma_f32 v[98:99], v[198:199], v[132:133], v[98:99] op_sel_hi:[0,1,1]
	v_pk_fma_f32 v[100:101], v[214:215], v[132:133], v[100:101] op_sel_hi:[0,1,1]
	v_pk_fma_f32 v[102:103], v[230:231], v[132:133], v[102:103] op_sel_hi:[0,1,1]
	v_pk_fma_f32 v[96:97], v[182:183], v[134:135], v[96:97] op_sel:[1,0,0]
	v_pk_fma_f32 v[98:99], v[198:199], v[134:135], v[98:99] op_sel:[1,0,0]
	v_pk_fma_f32 v[100:101], v[214:215], v[134:135], v[100:101] op_sel:[1,0,0]
	v_pk_fma_f32 v[102:103], v[230:231], v[134:135], v[102:103] op_sel:[1,0,0]
	global_load_dwordx2 v[104:105], v[232:233], off
	global_load_dwordx2 v[106:107], v[232:233], off offset:512
	global_load_dwordx2 v[108:109], v[232:233], off offset:1024
	global_load_dwordx2 v[110:111], v[232:233], off offset:1536
	global_load_dwordx2 v[112:113], v[232:233], off offset:2048
	global_load_dwordx2 v[114:115], v[232:233], off offset:2560
	global_load_dwordx2 v[116:117], v[232:233], off offset:3072
	global_load_dwordx2 v[118:119], v[232:233], off offset:3584
	v_lshl_add_u64 v[232:233], v[232:233], 0, s[6:7]
	global_load_dwordx2 v[120:121], v[232:233], off
	global_load_dwordx2 v[122:123], v[232:233], off offset:512
	global_load_dwordx2 v[124:125], v[232:233], off offset:1024
	global_load_dwordx2 v[126:127], v[232:233], off offset:1536
	global_load_dwordx2 v[128:129], v[232:233], off offset:2048
	global_load_dwordx2 v[130:131], v[232:233], off offset:2560
	global_load_dwordx2 v[132:133], v[232:233], off offset:3072
	global_load_dwordx2 v[134:135], v[232:233], off offset:3584
	v_lshl_add_u64 v[232:233], v[232:233], 0, s[6:7]
	ds_read_b128 v[168:171], v235 offset:192
	ds_read_b128 v[172:175], v235 offset:208
	ds_read_b128 v[176:179], v235 offset:224
	ds_read_b128 v[180:183], v235 offset:240
	ds_read_b128 v[184:187], v235 offset:704
	ds_read_b128 v[188:191], v235 offset:720
	ds_read_b128 v[192:195], v235 offset:736
	ds_read_b128 v[196:199], v235 offset:752
	ds_read_b128 v[200:203], v235 offset:1216
	ds_read_b128 v[204:207], v235 offset:1232
	ds_read_b128 v[208:211], v235 offset:1248
	ds_read_b128 v[212:215], v235 offset:1264
	ds_read_b128 v[216:219], v235 offset:1728
	ds_read_b128 v[220:223], v235 offset:1744
	ds_read_b128 v[224:227], v235 offset:1760
	ds_read_b128 v[228:231], v235 offset:1776
	s_waitcnt vmcnt(16)
; __device__ __forceinline__ void cmp_finalize_phase(Frame& F) {
;     ...
;         float a0 = 0.f, a1 = 0.f;
; #pragma unroll 8
;         for (int n = 0; n < 128; ++n) { const float h = hl[n]; a0 += h * w2[n * 128 + F.lane]; a1 += h * w2[n * 128 + 64 + F.lane]; }
	s_waitcnt lgkmcnt(0)
	v_pk_fma_f32 v[96:97], v[168:169], v[136:137], v[96:97] op_sel_hi:[0,1,1]
	v_pk_fma_f32 v[98:99], v[184:185], v[136:137], v[98:99] op_sel_hi:[0,1,1]
	v_pk_fma_f32 v[100:101], v[200:201], v[136:137], v[100:101] op_sel_hi:[0,1,1]
	v_pk_fma_f32 v[102:103], v[216:217], v[136:137], v[102:103] op_sel_hi:[0,1,1]
	v_pk_fma_f32 v[96:97], v[168:169], v[138:139], v[96:97] op_sel:[1,0,0]
	v_pk_fma_f32 v[98:99], v[184:185], v[138:139], v[98:99] op_sel:[1,0,0]
	v_pk_fma_f32 v[100:101], v[200:201], v[138:139], v[100:101] op_sel:[1,0,0]
	v_pk_fma_f32 v[102:103], v[216:217], v[138:139], v[102:103] op_sel:[1,0,0]
	v_pk_fma_f32 v[96:97], v[170:171], v[140:141], v[96:97] op_sel_hi:[0,1,1]
	v_pk_fma_f32 v[98:99], v[186:187], v[140:141], v[98:99] op_sel_hi:[0,1,1]
	v_pk_fma_f32 v[100:101], v[202:203], v[140:141], v[100:101] op_sel_hi:[0,1,1]
	v_pk_fma_f32 v[102:103], v[218:219], v[140:141], v[102:103] op_sel_hi:[0,1,1]
	v_pk_fma_f32 v[96:97], v[170:171], v[142:143], v[96:97] op_sel:[1,0,0]
	v_pk_fma_f32 v[98:99], v[186:187], v[142:143], v[98:99] op_sel:[1,0,0]
	v_pk_fma_f32 v[100:101], v[202:203], v[142:143], v[100:101] op_sel:[1,0,0]
	v_pk_fma_f32 v[102:103], v[218:219], v[142:143], v[102:103] op_sel:[1,0,0]
	v_pk_fma_f32 v[96:97], v[172:173], v[144:145], v[96:97] op_sel_hi:[0,1,1]
	v_pk_fma_f32 v[98:99], v[188:189], v[144:145], v[98:99] op_sel_hi:[0,1,1]
	v_pk_fma_f32 v[100:101], v[204:205], v[144:145], v[100:101] op_sel_hi:[0,1,1]
	v_pk_fma_f32 v[102:103], v[220:221], v[144:145], v[102:103] op_sel_hi:[0,1,1]
	v_pk_fma_f32 v[96:97], v[172:173], v[146:147], v[96:97] op_sel:[1,0,0]
	v_pk_fma_f32 v[98:99], v[188:189], v[146:147], v[98:99] op_sel:[1,0,0]
	v_pk_fma_f32 v[100:101], v[204:205], v[146:147], v[100:101] op_sel:[1,0,0]
	v_pk_fma_f32 v[102:103], v[220:221], v[146:147], v[102:103] op_sel:[1,0,0]
	v_pk_fma_f32 v[96:97], v[174:175], v[148:149], v[96:97] op_sel_hi:[0,1,1]
	v_pk_fma_f32 v[98:99], v[190:191], v[148:149], v[98:99] op_sel_hi:[0,1,1]
	v_pk_fma_f32 v[100:101], v[206:207], v[148:149], v[100:101] op_sel_hi:[0,1,1]
	v_pk_fma_f32 v[102:103], v[222:223], v[148:149], v[102:103] op_sel_hi:[0,1,1]
	v_pk_fma_f32 v[96:97], v[174:175], v[150:151], v[96:97] op_sel:[1,0,0]
	v_pk_fma_f32 v[98:99], v[190:191], v[150:151], v[98:99] op_sel:[1,0,0]
	v_pk_fma_f32 v[100:101], v[206:207], v[150:151], v[100:101] op_sel:[1,0,0]
	v_pk_fma_f32 v[102:103], v[222:223], v[150:151], v[102:103] op_sel:[1,0,0]
	v_pk_fma_f32 v[96:97], v[176:177], v[152:153], v[96:97] op_sel_hi:[0,1,1]
	v_pk_fma_f32 v[98:99], v[192:193], v[152:153], v[98:99] op_sel_hi:[0,1,1]
	v_pk_fma_f32 v[100:101], v[208:209], v[152:153], v[100:101] op_sel_hi:[0,1,1]
	v_pk_fma_f32 v[102:103], v[224:225], v[152:153], v[102:103] op_sel_hi:[0,1,1]
	v_pk_fma_f32 v[96:97], v[176:177], v[154:155], v[96:97] op_sel:[1,0,0]
	v_pk_fma_f32 v[98:99], v[192:193], v[154:155], v[98:99] op_sel:[1,0,0]
	v_pk_fma_f32 v[100:101], v[208:209], v[154:155], v[100:101] op_sel:[1,0,0]
	v_pk_fma_f32 v[102:103], v[224:225], v[154:155], v[102:103] op_sel:[1,0,0]
	v_pk_fma_f32 v[96:97], v[178:179], v[156:157], v[96:97] op_sel_hi:[0,1,1]
	v_pk_fma_f32 v[98:99], v[194:195], v[156:157], v[98:99] op_sel_hi:[0,1,1]
	v_pk_fma_f32 v[100:101], v[210:211], v[156:157], v[100:101] op_sel_hi:[0,1,1]
	v_pk_fma_f32 v[102:103], v[226:227], v[156:157], v[102:103] op_sel_hi:[0,1,1]
	v_pk_fma_f32 v[96:97], v[178:179], v[158:159], v[96:97] op_sel:[1,0,0]
	v_pk_fma_f32 v[98:99], v[194:195], v[158:159], v[98:99] op_sel:[1,0,0]
	v_pk_fma_f32 v[100:101], v[210:211], v[158:159], v[100:101] op_sel:[1,0,0]
	v_pk_fma_f32 v[102:103], v[226:227], v[158:159], v[102:103] op_sel:[1,0,0]
	v_pk_fma_f32 v[96:97], v[180:181], v[160:161], v[96:97] op_sel_hi:[0,1,1]
	v_pk_fma_f32 v[98:99], v[196:197], v[160:161], v[98:99] op_sel_hi:[0,1,1]
	v_pk_fma_f32 v[100:101], v[212:213], v[160:161], v[100:101] op_sel_hi:[0,1,1]
	v_pk_fma_f32 v[102:103], v[228:229], v[160:161], v[102:103] op_sel_hi:[0,1,1]
	v_pk_fma_f32 v[96:97], v[180:181], v[162:163], v[96:97] op_sel:[1,0,0]
	v_pk_fma_f32 v[98:99], v[196:197], v[162:163], v[98:99] op_sel:[1,0,0]
	v_pk_fma_f32 v[100:101], v[212:213], v[162:163], v[100:101] op_sel:[1,0,0]
	v_pk_fma_f32 v[102:103], v[228:229], v[162:163], v[102:103] op_sel:[1,0,0]
	v_pk_fma_f32 v[96:97], v[182:183], v[164:165], v[96:97] op_sel_hi:[0,1,1]
	v_pk_fma_f32 v[98:99], v[198:199], v[164:165], v[98:99] op_sel_hi:[0,1,1]
	v_pk_fma_f32 v[100:101], v[214:215], v[164:165], v[100:101] op_sel_hi:[0,1,1]
	v_pk_fma_f32 v[102:103], v[230:231], v[164:165], v[102:103] op_sel_hi:[0,1,1]
	v_pk_fma_f32 v[96:97], v[182:183], v[166:167], v[96:97] op_sel:[1,0,0]
	v_pk_fma_f32 v[98:99], v[198:199], v[166:167], v[98:99] op_sel:[1,0,0]
	v_pk_fma_f32 v[100:101], v[214:215], v[166:167], v[100:101] op_sel:[1,0,0]
	v_pk_fma_f32 v[102:103], v[230:231], v[166:167], v[102:103] op_sel:[1,0,0]
	global_load_dwordx2 v[136:137], v[232:233], off
	global_load_dwordx2 v[138:139], v[232:233], off offset:512
	global_load_dwordx2 v[140:141], v[232:233], off offset:1024
	global_load_dwordx2 v[142:143], v[232:233], off offset:1536
	global_load_dwordx2 v[144:145], v[232:233], off offset:2048
	global_load_dwordx2 v[146:147], v[232:233], off offset:2560
	global_load_dwordx2 v[148:149], v[232:233], off offset:3072
	global_load_dwordx2 v[150:151], v[232:233], off offset:3584
	v_lshl_add_u64 v[232:233], v[232:233], 0, s[6:7]
	global_load_dwordx2 v[152:153], v[232:233], off
	global_load_dwordx2 v[154:155], v[232:233], off offset:512
	global_load_dwordx2 v[156:157], v[232:233], off offset:1024
	global_load_dwordx2 v[158:159], v[232:233], off offset:1536
	global_load_dwordx2 v[160:161], v[232:233], off offset:2048
	global_load_dwordx2 v[162:163], v[232:233], off offset:2560
	global_load_dwordx2 v[164:165], v[232:233], off offset:3072
	global_load_dwordx2 v[166:167], v[232:233], off offset:3584
	v_lshl_add_u64 v[232:233], v[232:233], 0, s[6:7]
	ds_read_b128 v[168:171], v235 offset:256
	ds_read_b128 v[172:175], v235 offset:272
	ds_read_b128 v[176:179], v235 offset:288
	ds_read_b128 v[180:183], v235 offset:304
	ds_read_b128 v[184:187], v235 offset:768
	ds_read_b128 v[188:191], v235 offset:784
	ds_read_b128 v[192:195], v235 offset:800
	ds_read_b128 v[196:199], v235 offset:816
	ds_read_b128 v[200:203], v235 offset:1280
	ds_read_b128 v[204:207], v235 offset:1296
	ds_read_b128 v[208:211], v235 offset:1312
	ds_read_b128 v[212:215], v235 offset:1328
	ds_read_b128 v[216:219], v235 offset:1792
	ds_read_b128 v[220:223], v235 offset:1808
	ds_read_b128 v[224:227], v235 offset:1824
	ds_read_b128 v[228:231], v235 offset:1840
	s_waitcnt vmcnt(16)
; __device__ __forceinline__ void cmp_finalize_phase(Frame& F) {
;     ...
;         float a0 = 0.f, a1 = 0.f;
; #pragma unroll 8
;         for (int n = 0; n < 128; ++n) { const float h = hl[n]; a0 += h * w2[n * 128 + F.lane]; a1 += h * w2[n * 128 + 64 + F.lane]; }
	s_waitcnt lgkmcnt(0)
	v_pk_fma_f32 v[96:97], v[168:169], v[104:105], v[96:97] op_sel_hi:[0,1,1]
	v_pk_fma_f32 v[98:99], v[184:185], v[104:105], v[98:99] op_sel_hi:[0,1,1]
	v_pk_fma_f32 v[100:101], v[200:201], v[104:105], v[100:101] op_sel_hi:[0,1,1]
	v_pk_fma_f32 v[102:103], v[216:217], v[104:105], v[102:103] op_sel_hi:[0,1,1]
	v_pk_fma_f32 v[96:97], v[168:169], v[106:107], v[96:97] op_sel:[1,0,0]
	v_pk_fma_f32 v[98:99], v[184:185], v[106:107], v[98:99] op_sel:[1,0,0]
	v_pk_fma_f32 v[100:101], v[200:201], v[106:107], v[100:101] op_sel:[1,0,0]
	v_pk_fma_f32 v[102:103], v[216:217], v[106:107], v[102:103] op_sel:[1,0,0]
	v_pk_fma_f32 v[96:97], v[170:171], v[108:109], v[96:97] op_sel_hi:[0,1,1]
	v_pk_fma_f32 v[98:99], v[186:187], v[108:109], v[98:99] op_sel_hi:[0,1,1]
	v_pk_fma_f32 v[100:101], v[202:203], v[108:109], v[100:101] op_sel_hi:[0,1,1]
	v_pk_fma_f32 v[102:103], v[218:219], v[108:109], v[102:103] op_sel_hi:[0,1,1]
	v_pk_fma_f32 v[96:97], v[170:171], v[110:111], v[96:97] op_sel:[1,0,0]
	v_pk_fma_f32 v[98:99], v[186:187], v[110:111], v[98:99] op_sel:[1,0,0]
	v_pk_fma_f32 v[100:101], v[202:203], v[110:111], v[100:101] op_sel:[1,0,0]
	v_pk_fma_f32 v[102:103], v[218:219], v[110:111], v[102:103] op_sel:[1,0,0]
	v_pk_fma_f32 v[96:97], v[172:173], v[112:113], v[96:97] op_sel_hi:[0,1,1]
	v_pk_fma_f32 v[98:99], v[188:189], v[112:113], v[98:99] op_sel_hi:[0,1,1]
	v_pk_fma_f32 v[100:101], v[204:205], v[112:113], v[100:101] op_sel_hi:[0,1,1]
	v_pk_fma_f32 v[102:103], v[220:221], v[112:113], v[102:103] op_sel_hi:[0,1,1]
	v_pk_fma_f32 v[96:97], v[172:173], v[114:115], v[96:97] op_sel:[1,0,0]
	v_pk_fma_f32 v[98:99], v[188:189], v[114:115], v[98:99] op_sel:[1,0,0]
	v_pk_fma_f32 v[100:101], v[204:205], v[114:115], v[100:101] op_sel:[1,0,0]
	v_pk_fma_f32 v[102:103], v[220:221], v[114:115], v[102:103] op_sel:[1,0,0]
	v_pk_fma_f32 v[96:97], v[174:175], v[116:117], v[96:97] op_sel_hi:[0,1,1]
	v_pk_fma_f32 v[98:99], v[190:191], v[116:117], v[98:99] op_sel_hi:[0,1,1]
	v_pk_fma_f32 v[100:101], v[206:207], v[116:117], v[100:101] op_sel_hi:[0,1,1]
	v_pk_fma_f32 v[102:103], v[222:223], v[116:117], v[102:103] op_sel_hi:[0,1,1]
	v_pk_fma_f32 v[96:97], v[174:175], v[118:119], v[96:97] op_sel:[1,0,0]
	v_pk_fma_f32 v[98:99], v[190:191], v[118:119], v[98:99] op_sel:[1,0,0]
	v_pk_fma_f32 v[100:101], v[206:207], v[118:119], v[100:101] op_sel:[1,0,0]
	v_pk_fma_f32 v[102:103], v[222:223], v[118:119], v[102:103] op_sel:[1,0,0]
	v_pk_fma_f32 v[96:97], v[176:177], v[120:121], v[96:97] op_sel_hi:[0,1,1]
	v_pk_fma_f32 v[98:99], v[192:193], v[120:121], v[98:99] op_sel_hi:[0,1,1]
	v_pk_fma_f32 v[100:101], v[208:209], v[120:121], v[100:101] op_sel_hi:[0,1,1]
	v_pk_fma_f32 v[102:103], v[224:225], v[120:121], v[102:103] op_sel_hi:[0,1,1]
	v_pk_fma_f32 v[96:97], v[176:177], v[122:123], v[96:97] op_sel:[1,0,0]
	v_pk_fma_f32 v[98:99], v[192:193], v[122:123], v[98:99] op_sel:[1,0,0]
	v_pk_fma_f32 v[100:101], v[208:209], v[122:123], v[100:101] op_sel:[1,0,0]
	v_pk_fma_f32 v[102:103], v[224:225], v[122:123], v[102:103] op_sel:[1,0,0]
	v_pk_fma_f32 v[96:97], v[178:179], v[124:125], v[96:97] op_sel_hi:[0,1,1]
	v_pk_fma_f32 v[98:99], v[194:195], v[124:125], v[98:99] op_sel_hi:[0,1,1]
	v_pk_fma_f32 v[100:101], v[210:211], v[124:125], v[100:101] op_sel_hi:[0,1,1]
	v_pk_fma_f32 v[102:103], v[226:227], v[124:125], v[102:103] op_sel_hi:[0,1,1]
	v_pk_fma_f32 v[96:97], v[178:179], v[126:127], v[96:97] op_sel:[1,0,0]
	v_pk_fma_f32 v[98:99], v[194:195], v[126:127], v[98:99] op_sel:[1,0,0]
	v_pk_fma_f32 v[100:101], v[210:211], v[126:127], v[100:101] op_sel:[1,0,0]
	v_pk_fma_f32 v[102:103], v[226:227], v[126:127], v[102:103] op_sel:[1,0,0]
	v_pk_fma_f32 v[96:97], v[180:181], v[128:129], v[96:97] op_sel_hi:[0,1,1]
	v_pk_fma_f32 v[98:99], v[196:197], v[128:129], v[98:99] op_sel_hi:[0,1,1]
	v_pk_fma_f32 v[100:101], v[212:213], v[128:129], v[100:101] op_sel_hi:[0,1,1]
	v_pk_fma_f32 v[102:103], v[228:229], v[128:129], v[102:103] op_sel_hi:[0,1,1]
	v_pk_fma_f32 v[96:97], v[180:181], v[130:131], v[96:97] op_sel:[1,0,0]
	v_pk_fma_f32 v[98:99], v[196:197], v[130:131], v[98:99] op_sel:[1,0,0]
	v_pk_fma_f32 v[100:101], v[212:213], v[130:131], v[100:101] op_sel:[1,0,0]
	v_pk_fma_f32 v[102:103], v[228:229], v[130:131], v[102:103] op_sel:[1,0,0]
	v_pk_fma_f32 v[96:97], v[182:183], v[132:133], v[96:97] op_sel_hi:[0,1,1]
	v_pk_fma_f32 v[98:99], v[198:199], v[132:133], v[98:99] op_sel_hi:[0,1,1]
	v_pk_fma_f32 v[100:101], v[214:215], v[132:133], v[100:101] op_sel_hi:[0,1,1]
	v_pk_fma_f32 v[102:103], v[230:231], v[132:133], v[102:103] op_sel_hi:[0,1,1]
	v_pk_fma_f32 v[96:97], v[182:183], v[134:135], v[96:97] op_sel:[1,0,0]
	v_pk_fma_f32 v[98:99], v[198:199], v[134:135], v[98:99] op_sel:[1,0,0]
	v_pk_fma_f32 v[100:101], v[214:215], v[134:135], v[100:101] op_sel:[1,0,0]
	v_pk_fma_f32 v[102:103], v[230:231], v[134:135], v[102:103] op_sel:[1,0,0]
	global_load_dwordx2 v[104:105], v[232:233], off
	global_load_dwordx2 v[106:107], v[232:233], off offset:512
	global_load_dwordx2 v[108:109], v[232:233], off offset:1024
	global_load_dwordx2 v[110:111], v[232:233], off offset:1536
	global_load_dwordx2 v[112:113], v[232:233], off offset:2048
	global_load_dwordx2 v[114:115], v[232:233], off offset:2560
	global_load_dwordx2 v[116:117], v[232:233], off offset:3072
	global_load_dwordx2 v[118:119], v[232:233], off offset:3584
	v_lshl_add_u64 v[232:233], v[232:233], 0, s[6:7]
	global_load_dwordx2 v[120:121], v[232:233], off
	global_load_dwordx2 v[122:123], v[232:233], off offset:512
	global_load_dwordx2 v[124:125], v[232:233], off offset:1024
	global_load_dwordx2 v[126:127], v[232:233], off offset:1536
	global_load_dwordx2 v[128:129], v[232:233], off offset:2048
	global_load_dwordx2 v[130:131], v[232:233], off offset:2560
	global_load_dwordx2 v[132:133], v[232:233], off offset:3072
	global_load_dwordx2 v[134:135], v[232:233], off offset:3584
	v_lshl_add_u64 v[232:233], v[232:233], 0, s[6:7]
	ds_read_b128 v[168:171], v235 offset:320
	ds_read_b128 v[172:175], v235 offset:336
	ds_read_b128 v[176:179], v235 offset:352
	ds_read_b128 v[180:183], v235 offset:368
	ds_read_b128 v[184:187], v235 offset:832
	ds_read_b128 v[188:191], v235 offset:848
	ds_read_b128 v[192:195], v235 offset:864
	ds_read_b128 v[196:199], v235 offset:880
	ds_read_b128 v[200:203], v235 offset:1344
	ds_read_b128 v[204:207], v235 offset:1360
	ds_read_b128 v[208:211], v235 offset:1376
	ds_read_b128 v[212:215], v235 offset:1392
	ds_read_b128 v[216:219], v235 offset:1856
	ds_read_b128 v[220:223], v235 offset:1872
	ds_read_b128 v[224:227], v235 offset:1888
	ds_read_b128 v[228:231], v235 offset:1904
	s_waitcnt vmcnt(16)
; __device__ __forceinline__ void cmp_finalize_phase(Frame& F) {
;     ...
;         float a0 = 0.f, a1 = 0.f;
; #pragma unroll 8
;         for (int n = 0; n < 128; ++n) { const float h = hl[n]; a0 += h * w2[n * 128 + F.lane]; a1 += h * w2[n * 128 + 64 + F.lane]; }
	s_waitcnt lgkmcnt(0)
	v_pk_fma_f32 v[96:97], v[168:169], v[136:137], v[96:97] op_sel_hi:[0,1,1]
	v_pk_fma_f32 v[98:99], v[184:185], v[136:137], v[98:99] op_sel_hi:[0,1,1]
	v_pk_fma_f32 v[100:101], v[200:201], v[136:137], v[100:101] op_sel_hi:[0,1,1]
	v_pk_fma_f32 v[102:103], v[216:217], v[136:137], v[102:103] op_sel_hi:[0,1,1]
	v_pk_fma_f32 v[96:97], v[168:169], v[138:139], v[96:97] op_sel:[1,0,0]
	v_pk_fma_f32 v[98:99], v[184:185], v[138:139], v[98:99] op_sel:[1,0,0]
	v_pk_fma_f32 v[100:101], v[200:201], v[138:139], v[100:101] op_sel:[1,0,0]
	v_pk_fma_f32 v[102:103], v[216:217], v[138:139], v[102:103] op_sel:[1,0,0]
	v_pk_fma_f32 v[96:97], v[170:171], v[140:141], v[96:97] op_sel_hi:[0,1,1]
	v_pk_fma_f32 v[98:99], v[186:187], v[140:141], v[98:99] op_sel_hi:[0,1,1]
	v_pk_fma_f32 v[100:101], v[202:203], v[140:141], v[100:101] op_sel_hi:[0,1,1]
	v_pk_fma_f32 v[102:103], v[218:219], v[140:141], v[102:103] op_sel_hi:[0,1,1]
	v_pk_fma_f32 v[96:97], v[170:171], v[142:143], v[96:97] op_sel:[1,0,0]
	v_pk_fma_f32 v[98:99], v[186:187], v[142:143], v[98:99] op_sel:[1,0,0]
	v_pk_fma_f32 v[100:101], v[202:203], v[142:143], v[100:101] op_sel:[1,0,0]
	v_pk_fma_f32 v[102:103], v[218:219], v[142:143], v[102:103] op_sel:[1,0,0]
	v_pk_fma_f32 v[96:97], v[172:173], v[144:145], v[96:97] op_sel_hi:[0,1,1]
	v_pk_fma_f32 v[98:99], v[188:189], v[144:145], v[98:99] op_sel_hi:[0,1,1]
	v_pk_fma_f32 v[100:101], v[204:205], v[144:145], v[100:101] op_sel_hi:[0,1,1]
	v_pk_fma_f32 v[102:103], v[220:221], v[144:145], v[102:103] op_sel_hi:[0,1,1]
	v_pk_fma_f32 v[96:97], v[172:173], v[146:147], v[96:97] op_sel:[1,0,0]
	v_pk_fma_f32 v[98:99], v[188:189], v[146:147], v[98:99] op_sel:[1,0,0]
	v_pk_fma_f32 v[100:101], v[204:205], v[146:147], v[100:101] op_sel:[1,0,0]
	v_pk_fma_f32 v[102:103], v[220:221], v[146:147], v[102:103] op_sel:[1,0,0]
	v_pk_fma_f32 v[96:97], v[174:175], v[148:149], v[96:97] op_sel_hi:[0,1,1]
	v_pk_fma_f32 v[98:99], v[190:191], v[148:149], v[98:99] op_sel_hi:[0,1,1]
	v_pk_fma_f32 v[100:101], v[206:207], v[148:149], v[100:101] op_sel_hi:[0,1,1]
	v_pk_fma_f32 v[102:103], v[222:223], v[148:149], v[102:103] op_sel_hi:[0,1,1]
	v_pk_fma_f32 v[96:97], v[174:175], v[150:151], v[96:97] op_sel:[1,0,0]
	v_pk_fma_f32 v[98:99], v[190:191], v[150:151], v[98:99] op_sel:[1,0,0]
	v_pk_fma_f32 v[100:101], v[206:207], v[150:151], v[100:101] op_sel:[1,0,0]
	v_pk_fma_f32 v[102:103], v[222:223], v[150:151], v[102:103] op_sel:[1,0,0]
	v_pk_fma_f32 v[96:97], v[176:177], v[152:153], v[96:97] op_sel_hi:[0,1,1]
	v_pk_fma_f32 v[98:99], v[192:193], v[152:153], v[98:99] op_sel_hi:[0,1,1]
	v_pk_fma_f32 v[100:101], v[208:209], v[152:153], v[100:101] op_sel_hi:[0,1,1]
	v_pk_fma_f32 v[102:103], v[224:225], v[152:153], v[102:103] op_sel_hi:[0,1,1]
	v_pk_fma_f32 v[96:97], v[176:177], v[154:155], v[96:97] op_sel:[1,0,0]
	v_pk_fma_f32 v[98:99], v[192:193], v[154:155], v[98:99] op_sel:[1,0,0]
	v_pk_fma_f32 v[100:101], v[208:209], v[154:155], v[100:101] op_sel:[1,0,0]
	v_pk_fma_f32 v[102:103], v[224:225], v[154:155], v[102:103] op_sel:[1,0,0]
	v_pk_fma_f32 v[96:97], v[178:179], v[156:157], v[96:97] op_sel_hi:[0,1,1]
	v_pk_fma_f32 v[98:99], v[194:195], v[156:157], v[98:99] op_sel_hi:[0,1,1]
	v_pk_fma_f32 v[100:101], v[210:211], v[156:157], v[100:101] op_sel_hi:[0,1,1]
	v_pk_fma_f32 v[102:103], v[226:227], v[156:157], v[102:103] op_sel_hi:[0,1,1]
	v_pk_fma_f32 v[96:97], v[178:179], v[158:159], v[96:97] op_sel:[1,0,0]
	v_pk_fma_f32 v[98:99], v[194:195], v[158:159], v[98:99] op_sel:[1,0,0]
	v_pk_fma_f32 v[100:101], v[210:211], v[158:159], v[100:101] op_sel:[1,0,0]
	v_pk_fma_f32 v[102:103], v[226:227], v[158:159], v[102:103] op_sel:[1,0,0]
	v_pk_fma_f32 v[96:97], v[180:181], v[160:161], v[96:97] op_sel_hi:[0,1,1]
	v_pk_fma_f32 v[98:99], v[196:197], v[160:161], v[98:99] op_sel_hi:[0,1,1]
	v_pk_fma_f32 v[100:101], v[212:213], v[160:161], v[100:101] op_sel_hi:[0,1,1]
	v_pk_fma_f32 v[102:103], v[228:229], v[160:161], v[102:103] op_sel_hi:[0,1,1]
	v_pk_fma_f32 v[96:97], v[180:181], v[162:163], v[96:97] op_sel:[1,0,0]
	v_pk_fma_f32 v[98:99], v[196:197], v[162:163], v[98:99] op_sel:[1,0,0]
	v_pk_fma_f32 v[100:101], v[212:213], v[162:163], v[100:101] op_sel:[1,0,0]
	v_pk_fma_f32 v[102:103], v[228:229], v[162:163], v[102:103] op_sel:[1,0,0]
	v_pk_fma_f32 v[96:97], v[182:183], v[164:165], v[96:97] op_sel_hi:[0,1,1]
	v_pk_fma_f32 v[98:99], v[198:199], v[164:165], v[98:99] op_sel_hi:[0,1,1]
	v_pk_fma_f32 v[100:101], v[214:215], v[164:165], v[100:101] op_sel_hi:[0,1,1]
	v_pk_fma_f32 v[102:103], v[230:231], v[164:165], v[102:103] op_sel_hi:[0,1,1]
	v_pk_fma_f32 v[96:97], v[182:183], v[166:167], v[96:97] op_sel:[1,0,0]
	v_pk_fma_f32 v[98:99], v[198:199], v[166:167], v[98:99] op_sel:[1,0,0]
	v_pk_fma_f32 v[100:101], v[214:215], v[166:167], v[100:101] op_sel:[1,0,0]
	v_pk_fma_f32 v[102:103], v[230:231], v[166:167], v[102:103] op_sel:[1,0,0]
	global_load_dwordx2 v[136:137], v[232:233], off
	global_load_dwordx2 v[138:139], v[232:233], off offset:512
	global_load_dwordx2 v[140:141], v[232:233], off offset:1024
	global_load_dwordx2 v[142:143], v[232:233], off offset:1536
	global_load_dwordx2 v[144:145], v[232:233], off offset:2048
	global_load_dwordx2 v[146:147], v[232:233], off offset:2560
	global_load_dwordx2 v[148:149], v[232:233], off offset:3072
	global_load_dwordx2 v[150:151], v[232:233], off offset:3584
	v_lshl_add_u64 v[232:233], v[232:233], 0, s[6:7]
	global_load_dwordx2 v[152:153], v[232:233], off
	global_load_dwordx2 v[154:155], v[232:233], off offset:512
	global_load_dwordx2 v[156:157], v[232:233], off offset:1024
	global_load_dwordx2 v[158:159], v[232:233], off offset:1536
	global_load_dwordx2 v[160:161], v[232:233], off offset:2048
	global_load_dwordx2 v[162:163], v[232:233], off offset:2560
	global_load_dwordx2 v[164:165], v[232:233], off offset:3072
	global_load_dwordx2 v[166:167], v[232:233], off offset:3584
	v_lshl_add_u64 v[232:233], v[232:233], 0, s[6:7]
	ds_read_b128 v[168:171], v235 offset:384
	ds_read_b128 v[172:175], v235 offset:400
	ds_read_b128 v[176:179], v235 offset:416
	ds_read_b128 v[180:183], v235 offset:432
	ds_read_b128 v[184:187], v235 offset:896
	ds_read_b128 v[188:191], v235 offset:912
	ds_read_b128 v[192:195], v235 offset:928
	ds_read_b128 v[196:199], v235 offset:944
	ds_read_b128 v[200:203], v235 offset:1408
	ds_read_b128 v[204:207], v235 offset:1424
	ds_read_b128 v[208:211], v235 offset:1440
	ds_read_b128 v[212:215], v235 offset:1456
	ds_read_b128 v[216:219], v235 offset:1920
	ds_read_b128 v[220:223], v235 offset:1936
	ds_read_b128 v[224:227], v235 offset:1952
	ds_read_b128 v[228:231], v235 offset:1968
	s_waitcnt vmcnt(16)
; __device__ __forceinline__ void cmp_finalize_phase(Frame& F) {
;     ...
;         float a0 = 0.f, a1 = 0.f;
; #pragma unroll 8
;         for (int n = 0; n < 128; ++n) { const float h = hl[n]; a0 += h * w2[n * 128 + F.lane]; a1 += h * w2[n * 128 + 64 + F.lane]; }
	s_waitcnt lgkmcnt(0)
	v_pk_fma_f32 v[96:97], v[168:169], v[104:105], v[96:97] op_sel_hi:[0,1,1]
	v_pk_fma_f32 v[98:99], v[184:185], v[104:105], v[98:99] op_sel_hi:[0,1,1]
	v_pk_fma_f32 v[100:101], v[200:201], v[104:105], v[100:101] op_sel_hi:[0,1,1]
	v_pk_fma_f32 v[102:103], v[216:217], v[104:105], v[102:103] op_sel_hi:[0,1,1]
	v_pk_fma_f32 v[96:97], v[168:169], v[106:107], v[96:97] op_sel:[1,0,0]
	v_pk_fma_f32 v[98:99], v[184:185], v[106:107], v[98:99] op_sel:[1,0,0]
	v_pk_fma_f32 v[100:101], v[200:201], v[106:107], v[100:101] op_sel:[1,0,0]
	v_pk_fma_f32 v[102:103], v[216:217], v[106:107], v[102:103] op_sel:[1,0,0]
	v_pk_fma_f32 v[96:97], v[170:171], v[108:109], v[96:97] op_sel_hi:[0,1,1]
	v_pk_fma_f32 v[98:99], v[186:187], v[108:109], v[98:99] op_sel_hi:[0,1,1]
	v_pk_fma_f32 v[100:101], v[202:203], v[108:109], v[100:101] op_sel_hi:[0,1,1]
	v_pk_fma_f32 v[102:103], v[218:219], v[108:109], v[102:103] op_sel_hi:[0,1,1]
	v_pk_fma_f32 v[96:97], v[170:171], v[110:111], v[96:97] op_sel:[1,0,0]
	v_pk_fma_f32 v[98:99], v[186:187], v[110:111], v[98:99] op_sel:[1,0,0]
	v_pk_fma_f32 v[100:101], v[202:203], v[110:111], v[100:101] op_sel:[1,0,0]
	v_pk_fma_f32 v[102:103], v[218:219], v[110:111], v[102:103] op_sel:[1,0,0]
	v_pk_fma_f32 v[96:97], v[172:173], v[112:113], v[96:97] op_sel_hi:[0,1,1]
	v_pk_fma_f32 v[98:99], v[188:189], v[112:113], v[98:99] op_sel_hi:[0,1,1]
	v_pk_fma_f32 v[100:101], v[204:205], v[112:113], v[100:101] op_sel_hi:[0,1,1]
	v_pk_fma_f32 v[102:103], v[220:221], v[112:113], v[102:103] op_sel_hi:[0,1,1]
	v_pk_fma_f32 v[96:97], v[172:173], v[114:115], v[96:97] op_sel:[1,0,0]
	v_pk_fma_f32 v[98:99], v[188:189], v[114:115], v[98:99] op_sel:[1,0,0]
	v_pk_fma_f32 v[100:101], v[204:205], v[114:115], v[100:101] op_sel:[1,0,0]
	v_pk_fma_f32 v[102:103], v[220:221], v[114:115], v[102:103] op_sel:[1,0,0]
	v_pk_fma_f32 v[96:97], v[174:175], v[116:117], v[96:97] op_sel_hi:[0,1,1]
	v_pk_fma_f32 v[98:99], v[190:191], v[116:117], v[98:99] op_sel_hi:[0,1,1]
	v_pk_fma_f32 v[100:101], v[206:207], v[116:117], v[100:101] op_sel_hi:[0,1,1]
	v_pk_fma_f32 v[102:103], v[222:223], v[116:117], v[102:103] op_sel_hi:[0,1,1]
	v_pk_fma_f32 v[96:97], v[174:175], v[118:119], v[96:97] op_sel:[1,0,0]
	v_pk_fma_f32 v[98:99], v[190:191], v[118:119], v[98:99] op_sel:[1,0,0]
	v_pk_fma_f32 v[100:101], v[206:207], v[118:119], v[100:101] op_sel:[1,0,0]
	v_pk_fma_f32 v[102:103], v[222:223], v[118:119], v[102:103] op_sel:[1,0,0]
	v_pk_fma_f32 v[96:97], v[176:177], v[120:121], v[96:97] op_sel_hi:[0,1,1]
	v_pk_fma_f32 v[98:99], v[192:193], v[120:121], v[98:99] op_sel_hi:[0,1,1]
	v_pk_fma_f32 v[100:101], v[208:209], v[120:121], v[100:101] op_sel_hi:[0,1,1]
	v_pk_fma_f32 v[102:103], v[224:225], v[120:121], v[102:103] op_sel_hi:[0,1,1]
	v_pk_fma_f32 v[96:97], v[176:177], v[122:123], v[96:97] op_sel:[1,0,0]
	v_pk_fma_f32 v[98:99], v[192:193], v[122:123], v[98:99] op_sel:[1,0,0]
	v_pk_fma_f32 v[100:101], v[208:209], v[122:123], v[100:101] op_sel:[1,0,0]
	v_pk_fma_f32 v[102:103], v[224:225], v[122:123], v[102:103] op_sel:[1,0,0]
	v_pk_fma_f32 v[96:97], v[178:179], v[124:125], v[96:97] op_sel_hi:[0,1,1]
	v_pk_fma_f32 v[98:99], v[194:195], v[124:125], v[98:99] op_sel_hi:[0,1,1]
	v_pk_fma_f32 v[100:101], v[210:211], v[124:125], v[100:101] op_sel_hi:[0,1,1]
	v_pk_fma_f32 v[102:103], v[226:227], v[124:125], v[102:103] op_sel_hi:[0,1,1]
	v_pk_fma_f32 v[96:97], v[178:179], v[126:127], v[96:97] op_sel:[1,0,0]
	v_pk_fma_f32 v[98:99], v[194:195], v[126:127], v[98:99] op_sel:[1,0,0]
	v_pk_fma_f32 v[100:101], v[210:211], v[126:127], v[100:101] op_sel:[1,0,0]
	v_pk_fma_f32 v[102:103], v[226:227], v[126:127], v[102:103] op_sel:[1,0,0]
	v_pk_fma_f32 v[96:97], v[180:181], v[128:129], v[96:97] op_sel_hi:[0,1,1]
	v_pk_fma_f32 v[98:99], v[196:197], v[128:129], v[98:99] op_sel_hi:[0,1,1]
	v_pk_fma_f32 v[100:101], v[212:213], v[128:129], v[100:101] op_sel_hi:[0,1,1]
	v_pk_fma_f32 v[102:103], v[228:229], v[128:129], v[102:103] op_sel_hi:[0,1,1]
	v_pk_fma_f32 v[96:97], v[180:181], v[130:131], v[96:97] op_sel:[1,0,0]
	v_pk_fma_f32 v[98:99], v[196:197], v[130:131], v[98:99] op_sel:[1,0,0]
	v_pk_fma_f32 v[100:101], v[212:213], v[130:131], v[100:101] op_sel:[1,0,0]
	v_pk_fma_f32 v[102:103], v[228:229], v[130:131], v[102:103] op_sel:[1,0,0]
	v_pk_fma_f32 v[96:97], v[182:183], v[132:133], v[96:97] op_sel_hi:[0,1,1]
	v_pk_fma_f32 v[98:99], v[198:199], v[132:133], v[98:99] op_sel_hi:[0,1,1]
	v_pk_fma_f32 v[100:101], v[214:215], v[132:133], v[100:101] op_sel_hi:[0,1,1]
	v_pk_fma_f32 v[102:103], v[230:231], v[132:133], v[102:103] op_sel_hi:[0,1,1]
	v_pk_fma_f32 v[96:97], v[182:183], v[134:135], v[96:97] op_sel:[1,0,0]
	v_pk_fma_f32 v[98:99], v[198:199], v[134:135], v[98:99] op_sel:[1,0,0]
	v_pk_fma_f32 v[100:101], v[214:215], v[134:135], v[100:101] op_sel:[1,0,0]
	v_pk_fma_f32 v[102:103], v[230:231], v[134:135], v[102:103] op_sel:[1,0,0]
	ds_read_b128 v[168:171], v235 offset:448
	ds_read_b128 v[172:175], v235 offset:464
	ds_read_b128 v[176:179], v235 offset:480
	ds_read_b128 v[180:183], v235 offset:496
	ds_read_b128 v[184:187], v235 offset:960
	ds_read_b128 v[188:191], v235 offset:976
	ds_read_b128 v[192:195], v235 offset:992
	ds_read_b128 v[196:199], v235 offset:1008
	ds_read_b128 v[200:203], v235 offset:1472
	ds_read_b128 v[204:207], v235 offset:1488
	ds_read_b128 v[208:211], v235 offset:1504
	ds_read_b128 v[212:215], v235 offset:1520
	ds_read_b128 v[216:219], v235 offset:1984
	ds_read_b128 v[220:223], v235 offset:2000
	ds_read_b128 v[224:227], v235 offset:2016
	ds_read_b128 v[228:231], v235 offset:2032
	s_waitcnt vmcnt(0)
	s_waitcnt lgkmcnt(0)
; __device__ __forceinline__ unsigned f2bf(float f) { unsigned u = __builtin_bit_cast(unsigned, f); return (u + 0x7fffu + ((u >> 16) & 1u)) >> 16; }
; __device__ __forceinline__ unsigned pk4_fp8(float a, float b, float c, float d) { unsigned w = 0u; w = __builtin_amdgcn_cvt_pk_fp8_f32(a, b, w, false); w = __builtin_amdgcn_cvt_pk_fp8_f32(c, d, w, true); return w; }
; __device__ __forceinline__ void cmp_finalize_phase(Frame& F) {
;     ...
;         for (int n = 0; n < 128; ++n) { const float h = hl[n]; a0 += h * w2[n * 128 + F.lane]; a1 += h * w2[n * 128 + 64 + F.lane]; }
;         if (which) { dst[F.lane] = (bf16)f2bf(a0); dst[F.lane + 64] = (bf16)f2bf(a1); }
;         else { const unsigned w8 = pk4_fp8(a0, a1, 0.f, 0.f); dst8[F.lane] = (unsigned char)(w8 & 0xffu); dst8[F.lane + 64] = (unsigned char)((w8 >> 8) & 0xffu); }
	v_pk_fma_f32 v[96:97], v[168:169], v[136:137], v[96:97] op_sel_hi:[0,1,1]
	v_pk_fma_f32 v[98:99], v[184:185], v[136:137], v[98:99] op_sel_hi:[0,1,1]
	v_pk_fma_f32 v[100:101], v[200:201], v[136:137], v[100:101] op_sel_hi:[0,1,1]
	v_pk_fma_f32 v[102:103], v[216:217], v[136:137], v[102:103] op_sel_hi:[0,1,1]
	v_pk_fma_f32 v[96:97], v[168:169], v[138:139], v[96:97] op_sel:[1,0,0]
	v_pk_fma_f32 v[98:99], v[184:185], v[138:139], v[98:99] op_sel:[1,0,0]
	v_pk_fma_f32 v[100:101], v[200:201], v[138:139], v[100:101] op_sel:[1,0,0]
	v_pk_fma_f32 v[102:103], v[216:217], v[138:139], v[102:103] op_sel:[1,0,0]
	v_pk_fma_f32 v[96:97], v[170:171], v[140:141], v[96:97] op_sel_hi:[0,1,1]
	v_pk_fma_f32 v[98:99], v[186:187], v[140:141], v[98:99] op_sel_hi:[0,1,1]
	v_pk_fma_f32 v[100:101], v[202:203], v[140:141], v[100:101] op_sel_hi:[0,1,1]
	v_pk_fma_f32 v[102:103], v[218:219], v[140:141], v[102:103] op_sel_hi:[0,1,1]
	v_pk_fma_f32 v[96:97], v[170:171], v[142:143], v[96:97] op_sel:[1,0,0]
	v_pk_fma_f32 v[98:99], v[186:187], v[142:143], v[98:99] op_sel:[1,0,0]
	v_pk_fma_f32 v[100:101], v[202:203], v[142:143], v[100:101] op_sel:[1,0,0]
	v_pk_fma_f32 v[102:103], v[218:219], v[142:143], v[102:103] op_sel:[1,0,0]
	v_pk_fma_f32 v[96:97], v[172:173], v[144:145], v[96:97] op_sel_hi:[0,1,1]
	v_pk_fma_f32 v[98:99], v[188:189], v[144:145], v[98:99] op_sel_hi:[0,1,1]
	v_pk_fma_f32 v[100:101], v[204:205], v[144:145], v[100:101] op_sel_hi:[0,1,1]
	v_pk_fma_f32 v[102:103], v[220:221], v[144:145], v[102:103] op_sel_hi:[0,1,1]
	v_pk_fma_f32 v[96:97], v[172:173], v[146:147], v[96:97] op_sel:[1,0,0]
	v_pk_fma_f32 v[98:99], v[188:189], v[146:147], v[98:99] op_sel:[1,0,0]
	v_pk_fma_f32 v[100:101], v[204:205], v[146:147], v[100:101] op_sel:[1,0,0]
	v_pk_fma_f32 v[102:103], v[220:221], v[146:147], v[102:103] op_sel:[1,0,0]
	v_pk_fma_f32 v[96:97], v[174:175], v[148:149], v[96:97] op_sel_hi:[0,1,1]
	v_pk_fma_f32 v[98:99], v[190:191], v[148:149], v[98:99] op_sel_hi:[0,1,1]
	v_pk_fma_f32 v[100:101], v[206:207], v[148:149], v[100:101] op_sel_hi:[0,1,1]
	v_pk_fma_f32 v[102:103], v[222:223], v[148:149], v[102:103] op_sel_hi:[0,1,1]
	v_pk_fma_f32 v[96:97], v[174:175], v[150:151], v[96:97] op_sel:[1,0,0]
	v_pk_fma_f32 v[98:99], v[190:191], v[150:151], v[98:99] op_sel:[1,0,0]
	v_pk_fma_f32 v[100:101], v[206:207], v[150:151], v[100:101] op_sel:[1,0,0]
	v_pk_fma_f32 v[102:103], v[222:223], v[150:151], v[102:103] op_sel:[1,0,0]
	v_pk_fma_f32 v[96:97], v[176:177], v[152:153], v[96:97] op_sel_hi:[0,1,1]
	v_pk_fma_f32 v[98:99], v[192:193], v[152:153], v[98:99] op_sel_hi:[0,1,1]
	v_pk_fma_f32 v[100:101], v[208:209], v[152:153], v[100:101] op_sel_hi:[0,1,1]
	v_pk_fma_f32 v[102:103], v[224:225], v[152:153], v[102:103] op_sel_hi:[0,1,1]
	v_pk_fma_f32 v[96:97], v[176:177], v[154:155], v[96:97] op_sel:[1,0,0]
	v_pk_fma_f32 v[98:99], v[192:193], v[154:155], v[98:99] op_sel:[1,0,0]
	v_pk_fma_f32 v[100:101], v[208:209], v[154:155], v[100:101] op_sel:[1,0,0]
	v_pk_fma_f32 v[102:103], v[224:225], v[154:155], v[102:103] op_sel:[1,0,0]
	v_pk_fma_f32 v[96:97], v[178:179], v[156:157], v[96:97] op_sel_hi:[0,1,1]
	v_pk_fma_f32 v[98:99], v[194:195], v[156:157], v[98:99] op_sel_hi:[0,1,1]
	v_pk_fma_f32 v[100:101], v[210:211], v[156:157], v[100:101] op_sel_hi:[0,1,1]
	v_pk_fma_f32 v[102:103], v[226:227], v[156:157], v[102:103] op_sel_hi:[0,1,1]
	v_pk_fma_f32 v[96:97], v[178:179], v[158:159], v[96:97] op_sel:[1,0,0]
	v_pk_fma_f32 v[98:99], v[194:195], v[158:159], v[98:99] op_sel:[1,0,0]
	v_pk_fma_f32 v[100:101], v[210:211], v[158:159], v[100:101] op_sel:[1,0,0]
	v_pk_fma_f32 v[102:103], v[226:227], v[158:159], v[102:103] op_sel:[1,0,0]
	v_pk_fma_f32 v[96:97], v[180:181], v[160:161], v[96:97] op_sel_hi:[0,1,1]
	v_pk_fma_f32 v[98:99], v[196:197], v[160:161], v[98:99] op_sel_hi:[0,1,1]
	v_pk_fma_f32 v[100:101], v[212:213], v[160:161], v[100:101] op_sel_hi:[0,1,1]
	v_pk_fma_f32 v[102:103], v[228:229], v[160:161], v[102:103] op_sel_hi:[0,1,1]
	v_pk_fma_f32 v[96:97], v[180:181], v[162:163], v[96:97] op_sel:[1,0,0]
	v_pk_fma_f32 v[98:99], v[196:197], v[162:163], v[98:99] op_sel:[1,0,0]
	v_pk_fma_f32 v[100:101], v[212:213], v[162:163], v[100:101] op_sel:[1,0,0]
	v_pk_fma_f32 v[102:103], v[228:229], v[162:163], v[102:103] op_sel:[1,0,0]
	v_pk_fma_f32 v[96:97], v[182:183], v[164:165], v[96:97] op_sel_hi:[0,1,1]
	v_pk_fma_f32 v[98:99], v[198:199], v[164:165], v[98:99] op_sel_hi:[0,1,1]
	v_pk_fma_f32 v[100:101], v[214:215], v[164:165], v[100:101] op_sel_hi:[0,1,1]
	v_pk_fma_f32 v[102:103], v[230:231], v[164:165], v[102:103] op_sel_hi:[0,1,1]
	v_pk_fma_f32 v[96:97], v[182:183], v[166:167], v[96:97] op_sel:[1,0,0]
	v_pk_fma_f32 v[98:99], v[198:199], v[166:167], v[98:99] op_sel:[1,0,0]
	v_pk_fma_f32 v[100:101], v[214:215], v[166:167], v[100:101] op_sel:[1,0,0]
	v_pk_fma_f32 v[102:103], v[230:231], v[166:167], v[102:103] op_sel:[1,0,0]
	s_cmp_eq_u32 s3, 0
	s_cbranch_scc0 .Lfin_out_v
	v_lshlrev_b32_e32 v236, 1, v32
	s_add_i32 s9, s8, 0
	s_lshl_b32 s10, s9, 7
	s_add_u32 s12, s18, s10
	s_addc_u32 s13, s19, 0
	s_and_b32 s9, s9, 0x3ff
	v_mov_b32_e32 v88, 0
	s_cmpk_eq_i32 s9, 0x3ff
	s_cbranch_scc1 .Lfin_k_st0
	v_cvt_pk_fp8_f32 v88, v96, v97
; __device__ __forceinline__ unsigned f2bf(float f) { unsigned u = __builtin_bit_cast(unsigned, f); return (u + 0x7fffu + ((u >> 16) & 1u)) >> 16; }
; __device__ __forceinline__ unsigned pk4_fp8(float a, float b, float c, float d) { unsigned w = 0u; w = __builtin_amdgcn_cvt_pk_fp8_f32(a, b, w, false); w = __builtin_amdgcn_cvt_pk_fp8_f32(c, d, w, true); return w; }
; __device__ __forceinline__ void cmp_finalize_phase(Frame& F) {
;     ...
;     for (int r = gw; r < 2 * 8 * 1024; r += NGW) {
;         const int which = r >> 13, i = r & 1023; bf16* dst = KC + (size_t)r * HD; unsigned char* dst8 = (unsigned char*)KC + (size_t)r * HD;
;         if (i == 1023) { if (which) { dst[F.lane] = 0; dst[F.lane + 64] = 0; } else { dst8[F.lane] = 0; dst8[F.lane + 64] = 0; } continue; }
;     ...
;         if (which) { dst[F.lane] = (bf16)f2bf(a0); dst[F.lane + 64] = (bf16)f2bf(a1); }
;         else { const unsigned w8 = pk4_fp8(a0, a1, 0.f, 0.f); dst8[F.lane] = (unsigned char)(w8 & 0xffu); dst8[F.lane + 64] = (unsigned char)((w8 >> 8) & 0xffu); }
.Lfin_k_st0:
	global_store_short v236, v88, s[12:13]
	s_add_i32 s9, s8, 2048
	s_lshl_b32 s10, s9, 7
	s_add_u32 s12, s18, s10
	s_addc_u32 s13, s19, 0
	s_and_b32 s9, s9, 0x3ff
	v_mov_b32_e32 v88, 0
	s_cmpk_eq_i32 s9, 0x3ff
	s_cbranch_scc1 .Lfin_k_st1
	v_cvt_pk_fp8_f32 v88, v98, v99
.Lfin_k_st1:
	global_store_short v236, v88, s[12:13]
	s_add_i32 s9, s8, 4096
	s_lshl_b32 s10, s9, 7
	s_add_u32 s12, s18, s10
	s_addc_u32 s13, s19, 0
	s_and_b32 s9, s9, 0x3ff
	v_mov_b32_e32 v88, 0
	s_cmpk_eq_i32 s9, 0x3ff
	s_cbranch_scc1 .Lfin_k_st2
	v_cvt_pk_fp8_f32 v88, v100, v101
.Lfin_k_st2:
	global_store_short v236, v88, s[12:13]
	s_add_i32 s9, s8, 6144
	s_lshl_b32 s10, s9, 7
	s_add_u32 s12, s18, s10
	s_addc_u32 s13, s19, 0
	s_and_b32 s9, s9, 0x3ff
	v_mov_b32_e32 v88, 0
	s_cmpk_eq_i32 s9, 0x3ff
	s_cbranch_scc1 .Lfin_k_st3
	v_cvt_pk_fp8_f32 v88, v102, v103
.Lfin_k_st3:
	global_store_short v236, v88, s[12:13]
	s_branch .Lfin_next
.Lfin_out_v:
	v_lshlrev_b32_e32 v236, 2, v32
	s_add_i32 s9, s8, 0
	s_lshl_b32 s10, s9, 8
	s_add_u32 s12, s18, s10
	s_addc_u32 s13, s19, 0
	s_and_b32 s9, s9, 0x3ff
	v_mov_b32_e32 v88, 0
	v_mov_b32_e32 v89, 0
	s_cmpk_eq_i32 s9, 0x3ff
	s_cbranch_scc1 .Lfin_v_st0
	v_bfe_u32 v88, v96, 16, 1
	v_bfe_u32 v89, v97, 16, 1
	v_add3_u32 v88, v96, v88, s25
	v_add3_u32 v89, v97, v89, s25
.Lfin_v_st0:
	global_store_short_d16_hi v236, v88, s[12:13]
	global_store_short_d16_hi v236, v89, s[12:13] offset:2
	s_add_i32 s9, s8, 2048
	s_lshl_b32 s10, s9, 8
	s_add_u32 s12, s18, s10
	s_addc_u32 s13, s19, 0
	s_and_b32 s9, s9, 0x3ff
	v_mov_b32_e32 v88, 0
	v_mov_b32_e32 v89, 0
	s_cmpk_eq_i32 s9, 0x3ff
	s_cbranch_scc1 .Lfin_v_st1
	v_bfe_u32 v88, v98, 16, 1
	v_bfe_u32 v89, v99, 16, 1
	v_add3_u32 v88, v98, v88, s25
	v_add3_u32 v89, v99, v89, s25
.Lfin_v_st1:
	global_store_short_d16_hi v236, v88, s[12:13]
	global_store_short_d16_hi v236, v89, s[12:13] offset:2
	s_add_i32 s9, s8, 4096
	s_lshl_b32 s10, s9, 8
	s_add_u32 s12, s18, s10
	s_addc_u32 s13, s19, 0
	s_and_b32 s9, s9, 0x3ff
	v_mov_b32_e32 v88, 0
	v_mov_b32_e32 v89, 0
	s_cmpk_eq_i32 s9, 0x3ff
	s_cbranch_scc1 .Lfin_v_st2
	v_bfe_u32 v88, v100, 16, 1
	v_bfe_u32 v89, v101, 16, 1
	v_add3_u32 v88, v100, v88, s25
	v_add3_u32 v89, v101, v89, s25
.Lfin_v_st2:
	global_store_short_d16_hi v236, v88, s[12:13]
	global_store_short_d16_hi v236, v89, s[12:13] offset:2
	s_add_i32 s9, s8, 6144
	s_lshl_b32 s10, s9, 8
	s_add_u32 s12, s18, s10
	s_addc_u32 s13, s19, 0
	s_and_b32 s9, s9, 0x3ff
	v_mov_b32_e32 v88, 0
	v_mov_b32_e32 v89, 0
	s_cmpk_eq_i32 s9, 0x3ff
	s_cbranch_scc1 .Lfin_v_st3
	v_bfe_u32 v88, v102, 16, 1
	v_bfe_u32 v89, v103, 16, 1
	v_add3_u32 v88, v102, v88, s25
	v_add3_u32 v89, v103, v89, s25
.Lfin_v_st3:
	global_store_short_d16_hi v236, v88, s[12:13]
	global_store_short_d16_hi v236, v89, s[12:13] offset:2
.Lfin_next:
	s_add_i32 s3, s3, 1
	s_cmp_lt_u32 s3, 2
	s_cbranch_scc1 .Lfin_pass
	s_branch .LBB0_1423

; #define GAS __attribute__((address_space(1)))
; #define FIN(i) kin(i)
; template <bool FINAL, bool ADDY = true>
; __device__ __forceinline__ void combine_phase(Frame& F, float* ssq_out) {
;     ...
;     for (int m = gw; m < T; m += NGW) {
;         const GAS u32x4* h4 = (const GAS u32x4*)(HB + (size_t)m * DM) + F.lane; const GAS u32x2* a4 = (const GAS u32x2*)(Y0 + (size_t)m * DM) + F.lane; const GAS u32x2* b4 = (const GAS u32x2*)(Y1 + (size_t)m * DM) + F.lane;
;         float v[4][8]; float s = 0.f;
; #pragma unroll
;         for (int j = 0; j < 4; ++j) { const u32x4 h = h4[64 * j]; u32x2 a = {0u, 0u}, b = {0u, 0u}; if (ADDY) { a = a4[64 * j]; b = b4[64 * j]; }
; #pragma unroll
;             for (int q = 0; q < 4; ++q) { const unsigned aw = q < 2 ? a.x : a.y, bw = q < 2 ? b.x : b.y;
;                 const f32x2 ya = (q & 1) ? __builtin_amdgcn_cvt_pk_f32_fp8((int)aw, true) : __builtin_amdgcn_cvt_pk_f32_fp8((int)aw, false), yb = (q & 1) ? __builtin_amdgcn_cvt_pk_f32_fp8((int)bw, true) : __builtin_amdgcn_cvt_pk_f32_fp8((int)bw, false);
;                 v[j][2 * q] = bf_lo(h[q]) + (ADDY ? (ya.x + yb.x) * (1.f / WD_SCALE) : 0.f); v[j][2 * q + 1] = bf_hi(h[q]) + (ADDY ? (ya.y + yb.y) * (1.f / WD_SCALE) : 0.f); } }
;         if constexpr (!FINAL) {
; #pragma unroll
;             for (int j = 0; j < 4; ++j) { u32x4 w;
; #pragma unroll
;                 for (int q = 0; q < 4; ++q) { w[q] = pk2(v[j][2 * q], v[j][2 * q + 1]); const float lo = bf_lo(w[q]), hi = bf_hi(w[q]); s += lo * lo + hi * hi; }
;                 ((GAS u32x4*)(HB + (size_t)m * DM) + F.lane)[64 * j] = w;
;                 u32x2 w8; w8.x = pk4_fp8(bf_lo(w.x), bf_hi(w.x), bf_lo(w.y), bf_hi(w.y)); w8.y = pk4_fp8(bf_lo(w.z), bf_hi(w.z), bf_lo(w.w), bf_hi(w.w));
;                 ((GAS u32x2*)(F.ws + WS_HB8 + (size_t)m * DM) + F.lane)[64 * j] = w8; }
;             s = wave_sum(s); if (F.lane == 0) ssq_out[m] = s;
;         } else {
; #pragma unroll
;             for (int j = 0; j < 4; ++j)
; #pragma unroll
;                 for (int q = 0; q < 8; ++q) s += v[j][q] * v[j][q];
;             s = wave_sum(s); const float rs = rstd_of(s);
;             const float* g = FIN(I_NFIN);
; #pragma unroll
;             for (int j = 0; j < 4; ++j) { const int c0 = 8 * F.lane + 512 * j; const f32x4 g0 = *(const f32x4*)(g + c0), g1 = *(const f32x4*)(g + c0 + 4);
.LBB0_2367:
	s_cmp_lt_i32 s92, 19
	s_cselect_b64 s[4:5], -1, 0
	s_and_b64 s[2:3], s[4:5], s[2:3]
	s_andn2_b64 vcc, exec, s[2:3]
	s_cbranch_vccnz .LBB0_2371
	s_lshl_b32 s2, s77, 3
	s_add_i32 s2, s2, s96
	s_cmpk_gt_i32 s2, 0x7fff
	s_cbranch_scc1 .LBB0_2371
	s_lshl_b32 s4, s33, 3
	s_ashr_i32 s3, s2, 31
	s_waitcnt vmcnt(0)
	v_ashrrev_i32_e32 v1, 31, v0
	s_lshl_b64 s[6:7], s[2:3], 12
	s_ashr_i32 s5, s4, 31
	v_lshl_add_u64 v[4:5], v[0:1], 4, s[6:7]
	s_lshl_b64 s[6:7], s[4:5], 12
	s_lshl_b64 s[8:9], s[2:3], 13
	v_lshlrev_b32_e32 v2, 3, v0
	s_add_u32 s8, s30, s8
	v_ashrrev_i32_e32 v3, 31, v2
	s_addc_u32 s9, s31, s9
	v_lshl_add_u64 v[6:7], v[2:3], 2, s[8:9]
	s_mov_b64 s[8:9], 0x1000
	s_lshl_b64 s[12:13], s[2:3], 11
	v_lshl_add_u64 v[6:7], v[6:7], 0, s[8:9]
	s_lshl_b64 s[10:11], s[4:5], 13
	v_lshl_add_u64 v[0:1], v[0:1], 3, s[12:13]
	s_lshl_b64 s[12:13], s[4:5], 11
	s_mov_b32 s14, 0x3d800000
	v_mov_b32_e32 v8, 0x358637bd
	s_movk_i32 s3, 0x1000
	s_mov_b64 s[16:17], 0x1800
	s_load_dwordx2 s[18:19], s[0:1], 0x58
	s_waitcnt lgkmcnt(0)
	v_lshl_add_u64 v[116:117], v[2:3], 2, s[18:19]
	v_lshl_add_u64 v[118:119], v[116:117], 0, s[8:9]
	global_load_dwordx4 v[120:123], v[116:117], off
	global_load_dwordx4 v[124:127], v[116:117], off offset:16
	global_load_dwordx4 v[128:131], v[116:117], off offset:2048
	global_load_dwordx4 v[132:135], v[116:117], off offset:2064
	global_load_dwordx4 v[136:139], v[118:119], off
	global_load_dwordx4 v[140:143], v[118:119], off offset:16
	global_load_dwordx4 v[144:147], v[118:119], off offset:2048
	global_load_dwordx4 v[148:151], v[118:119], off offset:2064
	s_waitcnt vmcnt(0)
.LBB0_2370:
	v_lshl_add_u64 v[10:11], s[28:29], 0, v[4:5]
	v_add_co_u32_e32 v28, vcc, 0x12000000, v10
	v_lshl_add_u64 v[26:27], s[28:29], 0, v[0:1]
	s_nop 0
	v_addc_co_u32_e32 v29, vcc, 0, v11, vcc
	v_add_co_u32_e32 v30, vcc, 0x1e800000, v26
	s_nop 0
	s_nop 0
	v_addc_co_u32_e32 v31, vcc, 0, v27, vcc
	v_add_co_u32_e32 v26, vcc, 0x22800000, v26
	global_load_dwordx4 v[10:13], v[28:29], off
	global_load_dwordx4 v[14:17], v[28:29], off offset:1024
	global_load_dwordx4 v[18:21], v[28:29], off offset:2048
	global_load_dwordx4 v[22:25], v[28:29], off offset:3072
	v_addc_co_u32_e32 v27, vcc, 0, v27, vcc
	s_waitcnt lgkmcnt(0)
	global_load_dwordx2 v[34:35], v[30:31], off
	global_load_dwordx2 v[36:37], v[30:31], off offset:512
	global_load_dwordx2 v[38:39], v[30:31], off offset:1024
	global_load_dwordx2 v[40:41], v[30:31], off offset:1536
	global_load_dwordx2 v[42:43], v[26:27], off
	global_load_dwordx2 v[44:45], v[26:27], off offset:512
	global_load_dwordx2 v[46:47], v[26:27], off offset:1024
	global_load_dwordx2 v[48:49], v[26:27], off offset:1536
	s_add_i32 s2, s2, s4
	v_lshl_add_u64 v[4:5], v[4:5], 0, s[6:7]
	v_lshl_add_u64 v[0:1], v[0:1], 0, s[12:13]
	s_cmp_lt_i32 s2, 0x8000
	s_waitcnt vmcnt(11)
	v_lshlrev_b32_e32 v52, 16, v12
	v_and_b32_e32 v53, 0xffff0000, v12
	v_lshlrev_b32_e32 v12, 16, v13
	s_waitcnt vmcnt(7)
	v_cvt_pk_f32_fp8_e32 v[68:69], v34
	v_cvt_pk_f32_fp8_sdwa v[70:71], v34 src0_sel:WORD_1
	v_cvt_pk_f32_fp8_e32 v[72:73], v35
	v_cvt_pk_f32_fp8_sdwa v[34:35], v35 src0_sel:WORD_1
	s_waitcnt vmcnt(3)
	v_cvt_pk_f32_fp8_e32 v[92:93], v42
	v_cvt_pk_f32_fp8_sdwa v[94:95], v42 src0_sel:WORD_1
	v_cvt_pk_f32_fp8_e32 v[96:97], v43
	v_cvt_pk_f32_fp8_sdwa v[42:43], v43 src0_sel:WORD_1
	v_cvt_pk_f32_fp8_e32 v[86:87], v40
	v_cvt_pk_f32_fp8_sdwa v[88:89], v40 src0_sel:WORD_1
	v_cvt_pk_f32_fp8_e32 v[90:91], v41
	v_cvt_pk_f32_fp8_sdwa v[40:41], v41 src0_sel:WORD_1
	s_waitcnt vmcnt(0)
	v_cvt_pk_f32_fp8_e32 v[110:111], v48
	v_cvt_pk_f32_fp8_sdwa v[112:113], v48 src0_sel:WORD_1
	v_cvt_pk_f32_fp8_e32 v[114:115], v49
	v_cvt_pk_f32_fp8_sdwa v[48:49], v49 src0_sel:WORD_1
	v_cvt_pk_f32_fp8_e32 v[74:75], v36
	v_cvt_pk_f32_fp8_sdwa v[76:77], v36 src0_sel:WORD_1
	v_cvt_pk_f32_fp8_e32 v[78:79], v37
	v_cvt_pk_f32_fp8_sdwa v[36:37], v37 src0_sel:WORD_1
	v_cvt_pk_f32_fp8_e32 v[98:99], v44
	v_cvt_pk_f32_fp8_sdwa v[100:101], v44 src0_sel:WORD_1
	v_cvt_pk_f32_fp8_e32 v[102:103], v45
	v_cvt_pk_f32_fp8_sdwa v[44:45], v45 src0_sel:WORD_1
	v_and_b32_e32 v13, 0xffff0000, v13
	v_lshlrev_b32_e32 v54, 16, v10
	v_and_b32_e32 v55, 0xffff0000, v10
	v_pk_add_f32 v[34:35], v[34:35], v[42:43]
	v_pk_add_f32 v[42:43], v[68:69], v[92:93]
	v_lshlrev_b32_e32 v10, 16, v11
	v_and_b32_e32 v11, 0xffff0000, v11
	v_lshlrev_b32_e32 v64, 16, v24
	v_and_b32_e32 v65, 0xffff0000, v24
	v_lshlrev_b32_e32 v24, 16, v25
	v_and_b32_e32 v25, 0xffff0000, v25
	v_lshlrev_b32_e32 v66, 16, v22
	v_and_b32_e32 v67, 0xffff0000, v22
	v_pk_add_f32 v[68:69], v[70:71], v[94:95]
	v_pk_add_f32 v[40:41], v[40:41], v[48:49]
	v_pk_add_f32 v[48:49], v[86:87], v[110:111]
	v_pk_fma_f32 v[12:13], v[34:35], s[14:15], v[12:13] op_sel_hi:[1,0,1]
	v_pk_fma_f32 v[34:35], v[42:43], s[14:15], v[54:55] op_sel_hi:[1,0,1]
	v_lshlrev_b32_e32 v58, 16, v14
	v_and_b32_e32 v59, 0xffff0000, v14
	v_pk_add_f32 v[36:37], v[36:37], v[44:45]
	v_pk_add_f32 v[44:45], v[74:75], v[98:99]
	v_pk_fma_f32 v[10:11], v[68:69], s[14:15], v[10:11] op_sel_hi:[1,0,1]
	v_pk_fma_f32 v[24:25], v[40:41], s[14:15], v[24:25] op_sel_hi:[1,0,1]
	v_pk_fma_f32 v[40:41], v[48:49], s[14:15], v[66:67] op_sel_hi:[1,0,1]
	v_pk_mul_f32 v[48:49], v[34:35], v[34:35]
	v_pk_add_f32 v[72:73], v[72:73], v[96:97]
	v_pk_fma_f32 v[44:45], v[44:45], s[14:15], v[58:59] op_sel_hi:[1,0,1]
	v_pk_mul_f32 v[58:59], v[10:11], v[10:11]
	v_add_f32_e32 v9, v48, v49
	v_lshlrev_b32_e32 v14, 16, v15
	v_and_b32_e32 v15, 0xffff0000, v15
	v_cvt_pk_f32_fp8_e32 v[80:81], v38
	v_cvt_pk_f32_fp8_sdwa v[82:83], v38 src0_sel:WORD_1
	v_cvt_pk_f32_fp8_e32 v[84:85], v39
	v_cvt_pk_f32_fp8_sdwa v[38:39], v39 src0_sel:WORD_1
; #define GAS __attribute__((address_space(1)))
; #define DPP_F(v, ctrl) __builtin_bit_cast(float, __builtin_amdgcn_mov_dpp(__builtin_bit_cast(int, (v)), (ctrl), 0xF, 0xF, true))
; __device__ __forceinline__ float xsum16(float v) { float a = v, b = v; PL_SWAP16(a, b); return a + b; }
; __device__ __forceinline__ float xsum32(float v) { float a = v, b = v; PL_SWAP32(a, b); return a + b; }
; __device__ __forceinline__ float rstd_of(float ssq) { return __builtin_amdgcn_rsqf(ssq * (1.0f / DM) + EPSN); }
; #define FIN(i) kin(i)
; __device__ __forceinline__ float wave_sum(float v) {
;     v += DPP_F(v, 0xB1); v += DPP_F(v, 0x4E); v += DPP_F(v, 0x141); v += DPP_F(v, 0x140);
;     return xsum32(xsum16(v));
; template <bool FINAL, bool ADDY = true>
; __device__ __forceinline__ void combine_phase(Frame& F, float* ssq_out) {
;     ...
; #pragma unroll
;             for (int j = 0; j < 4; ++j)
; #pragma unroll
;                 for (int q = 0; q < 8; ++q) s += v[j][q] * v[j][q];
;             s = wave_sum(s); const float rs = rstd_of(s);
;             const float* g = FIN(I_NFIN);
; #pragma unroll
;             for (int j = 0; j < 4; ++j) { const int c0 = 8 * F.lane + 512 * j; const f32x4 g0 = *(const f32x4*)(g + c0), g1 = *(const f32x4*)(g + c0 + 4);
;                 f32x4 o0 = {v[j][0] * rs * g0.x, v[j][1] * rs * g0.y, v[j][2] * rs * g0.z, v[j][3] * rs * g0.w}, o1 = {v[j][4] * rs * g1.x, v[j][5] * rs * g1.y, v[j][6] * rs * g1.z, v[j][7] * rs * g1.w};
;                 __builtin_nontemporal_store(o0, (GAS f32x4*)(F.out + (size_t)m * DM + c0)); __builtin_nontemporal_store(o1, (GAS f32x4*)(F.out + (size_t)m * DM + c0 + 4)); }
	v_cvt_pk_f32_fp8_e32 v[104:105], v46
	v_cvt_pk_f32_fp8_sdwa v[106:107], v46 src0_sel:WORD_1
	v_cvt_pk_f32_fp8_e32 v[108:109], v47
	v_cvt_pk_f32_fp8_sdwa v[46:47], v47 src0_sel:WORD_1
	v_pk_add_f32 v[74:75], v[76:77], v[100:101]
	v_pk_fma_f32 v[52:53], v[72:73], s[14:15], v[52:53] op_sel_hi:[1,0,1]
	v_add_f32_e32 v9, v9, v58
	v_pk_fma_f32 v[54:55], v[74:75], s[14:15], v[14:15] op_sel_hi:[1,0,1]
	v_pk_mul_f32 v[14:15], v[52:53], v[52:53]
	v_add_f32_e32 v9, v59, v9
	v_lshlrev_b32_e32 v56, 16, v16
	v_and_b32_e32 v57, 0xffff0000, v16
	v_lshlrev_b32_e32 v16, 16, v17
	v_and_b32_e32 v17, 0xffff0000, v17
	v_add_f32_e32 v9, v9, v14
	v_pk_fma_f32 v[36:37], v[36:37], s[14:15], v[16:17] op_sel_hi:[1,0,1]
	v_pk_mul_f32 v[16:17], v[12:13], v[12:13]
	v_add_f32_e32 v9, v15, v9
	v_lshlrev_b32_e32 v60, 16, v20
	v_and_b32_e32 v61, 0xffff0000, v20
	v_lshlrev_b32_e32 v20, 16, v21
	v_and_b32_e32 v21, 0xffff0000, v21
	v_lshlrev_b32_e32 v62, 16, v18
	v_and_b32_e32 v63, 0xffff0000, v18
	v_pk_add_f32 v[38:39], v[38:39], v[46:47]
	v_pk_add_f32 v[46:47], v[80:81], v[104:105]
	v_pk_add_f32 v[80:81], v[90:91], v[114:115]
	v_add_f32_e32 v9, v9, v16
	v_pk_fma_f32 v[20:21], v[38:39], s[14:15], v[20:21] op_sel_hi:[1,0,1]
	v_pk_fma_f32 v[38:39], v[46:47], s[14:15], v[62:63] op_sel_hi:[1,0,1]
	v_pk_fma_f32 v[46:47], v[80:81], s[14:15], v[64:65] op_sel_hi:[1,0,1]
	v_pk_mul_f32 v[64:65], v[44:45], v[44:45]
	v_add_f32_e32 v9, v17, v9
	v_add_f32_e32 v9, v9, v64
	v_pk_add_f32 v[70:71], v[78:79], v[102:103]
	v_pk_mul_f32 v[66:67], v[54:55], v[54:55]
	v_add_f32_e32 v9, v65, v9
	v_pk_add_f32 v[76:77], v[84:85], v[108:109]
	v_pk_fma_f32 v[42:43], v[70:71], s[14:15], v[56:57] op_sel_hi:[1,0,1]
	v_add_f32_e32 v9, v9, v66
	v_pk_fma_f32 v[56:57], v[76:77], s[14:15], v[60:61] op_sel_hi:[1,0,1]
	v_pk_mul_f32 v[60:61], v[42:43], v[42:43]
	v_add_f32_e32 v9, v67, v9
	v_add_f32_e32 v9, v9, v60
	v_pk_mul_f32 v[62:63], v[36:37], v[36:37]
	v_add_f32_e32 v9, v61, v9
	v_add_f32_e32 v9, v9, v62
	v_lshlrev_b32_e32 v18, 16, v19
	v_and_b32_e32 v19, 0xffff0000, v19
	v_pk_add_f32 v[78:79], v[82:83], v[106:107]
	v_pk_mul_f32 v[72:73], v[38:39], v[38:39]
	v_add_f32_e32 v9, v63, v9
	v_pk_fma_f32 v[18:19], v[78:79], s[14:15], v[18:19] op_sel_hi:[1,0,1]
	v_add_f32_e32 v9, v9, v72
	v_pk_mul_f32 v[74:75], v[18:19], v[18:19]
	v_add_f32_e32 v9, v73, v9
	v_add_f32_e32 v9, v9, v74
	v_pk_mul_f32 v[68:69], v[56:57], v[56:57]
	v_add_f32_e32 v9, v75, v9
	v_add_f32_e32 v9, v9, v68
	v_pk_mul_f32 v[70:71], v[20:21], v[20:21]
	v_add_f32_e32 v9, v69, v9
	v_add_f32_e32 v9, v9, v70
	v_lshlrev_b32_e32 v22, 16, v23
	v_and_b32_e32 v23, 0xffff0000, v23
	v_pk_add_f32 v[82:83], v[88:89], v[112:113]
	v_pk_mul_f32 v[80:81], v[40:41], v[40:41]
	v_add_f32_e32 v9, v71, v9
	v_pk_fma_f32 v[22:23], v[82:83], s[14:15], v[22:23] op_sel_hi:[1,0,1]
	v_add_f32_e32 v9, v9, v80
	v_pk_mul_f32 v[82:83], v[22:23], v[22:23]
	v_add_f32_e32 v9, v81, v9
	v_add_f32_e32 v9, v9, v82
	v_pk_mul_f32 v[76:77], v[46:47], v[46:47]
	v_add_f32_e32 v9, v83, v9
	v_add_f32_e32 v9, v9, v76
	v_pk_mul_f32 v[78:79], v[24:25], v[24:25]
	v_add_f32_e32 v9, v77, v9
	v_add_f32_e32 v9, v9, v78
	v_add_f32_e32 v9, v79, v9
	s_nop 1
	v_add_f32_dpp v9, v9, v9 quad_perm:[1,0,3,2] row_mask:0xf bank_mask:0xf bound_ctrl:1
	s_nop 1
	v_add_f32_dpp v9, v9, v9 quad_perm:[2,3,0,1] row_mask:0xf bank_mask:0xf bound_ctrl:1
	s_nop 1
	v_add_f32_dpp v9, v9, v9 row_half_mirror row_mask:0xf bank_mask:0xf bound_ctrl:1
	s_nop 1
	v_add_f32_dpp v9, v9, v9 row_mirror row_mask:0xf bank_mask:0xf bound_ctrl:1
	v_mov_b32_e32 v14, v9
	s_nop 1
	v_permlane16_swap_b32 v9, v14
	s_nop 0
	v_add_f32_e32 v9, v9, v14
	v_mov_b32_e32 v14, v9
	s_nop 1
	v_permlane32_swap_b32 v9, v14
	s_nop 0
	v_add_f32_e32 v9, v9, v14
	v_fmamk_f32 v9, v9, 0x3a000000, v8
	v_rsq_f32_e32 v48, v9
	s_nop 0
	v_pk_mul_f32 v[14:15], v[34:35], v[48:49] op_sel_hi:[1,0]
	v_pk_mul_f32 v[10:11], v[10:11], v[48:49] op_sel_hi:[1,0]
	v_pk_mul_f32 v[34:35], v[52:53], v[48:49] op_sel_hi:[1,0]
	v_pk_mul_f32 v[16:17], v[12:13], v[48:49] op_sel_hi:[1,0]
	v_pk_mul_f32 v[12:13], v[122:123], v[10:11]
	v_pk_mul_f32 v[10:11], v[120:121], v[14:15]
	v_pk_mul_f32 v[16:17], v[126:127], v[16:17]
	v_pk_mul_f32 v[14:15], v[124:125], v[34:35]
	global_store_dwordx4 v[6:7], v[10:13], off offset:-4096 nt
	global_store_dwordx4 v[6:7], v[14:17], off offset:-4080 nt
	v_pk_mul_f32 v[30:31], v[54:55], v[48:49] op_sel_hi:[1,0]
	v_pk_mul_f32 v[32:33], v[44:45], v[48:49] op_sel_hi:[1,0]
	v_pk_mul_f32 v[34:35], v[36:37], v[48:49] op_sel_hi:[1,0]
	v_pk_mul_f32 v[36:37], v[42:43], v[48:49] op_sel_hi:[1,0]
	v_pk_mul_f32 v[18:19], v[18:19], v[48:49] op_sel_hi:[1,0]
	v_pk_mul_f32 v[20:21], v[20:21], v[48:49] op_sel_hi:[1,0]
	v_pk_mul_f32 v[10:11], v[32:33], v[128:129]
	v_pk_mul_f32 v[12:13], v[30:31], v[130:131]
	v_pk_mul_f32 v[14:15], v[36:37], v[132:133]
	v_pk_mul_f32 v[16:17], v[34:35], v[134:135]
	global_store_dwordx4 v[6:7], v[10:13], off offset:-2048 nt
	global_store_dwordx4 v[6:7], v[14:17], off offset:-2032 nt
	v_pk_mul_f32 v[30:31], v[38:39], v[48:49] op_sel_hi:[1,0]
	v_pk_mul_f32 v[32:33], v[56:57], v[48:49] op_sel_hi:[1,0]
	v_pk_mul_f32 v[10:11], v[30:31], v[136:137]
	v_pk_mul_f32 v[12:13], v[18:19], v[138:139]
	v_pk_mul_f32 v[14:15], v[32:33], v[140:141]
	v_pk_mul_f32 v[16:17], v[20:21], v[142:143]
	global_store_dwordx4 v[6:7], v[10:13], off nt
	global_store_dwordx4 v[6:7], v[14:17], off offset:16 nt
	v_pk_mul_f32 v[18:19], v[22:23], v[48:49] op_sel_hi:[1,0]
	v_pk_mul_f32 v[20:21], v[40:41], v[48:49] op_sel_hi:[1,0]
	v_pk_mul_f32 v[22:23], v[24:25], v[48:49] op_sel_hi:[1,0]
	v_pk_mul_f32 v[24:25], v[46:47], v[48:49] op_sel_hi:[1,0]
	v_pk_mul_f32 v[10:11], v[20:21], v[144:145]
	v_pk_mul_f32 v[12:13], v[18:19], v[146:147]
	v_pk_mul_f32 v[14:15], v[24:25], v[148:149]
	v_pk_mul_f32 v[16:17], v[22:23], v[150:151]
	global_store_dwordx4 v[6:7], v[10:13], off offset:2048 nt
	global_store_dwordx4 v[6:7], v[14:17], off offset:2064 nt
	v_lshl_add_u64 v[6:7], v[6:7], 0, s[10:11]
	s_cbranch_scc1 .LBB0_2370
